# route reductions: xor-1/2/4/8 hops by DPP lane permutes and xor-16 hop by permlane16 swap instead of LDS lane shuffles (same pairing and order)
# baseline (speedup 1.0000x reference)
.LBB0_1875:
	s_lshl_b32 s87, s86, 5
	s_add_i32 s60, s87, s65
	s_ashr_i32 s61, s60, 31
	s_lshl_b64 s[34:35], s[60:61], 12
	v_lshl_add_u64 v[14:15], v[44:45], 0, s[34:35]
	v_lshl_add_u64 v[160:161], v[44:45], 0, s[34:35]
	global_load_dwordx4 v[2:5], v[14:15], off
	global_load_dwordx4 v[6:9], v[14:15], off offset:1024
	global_load_dwordx4 v[10:13], v[14:15], off offset:2048
	s_nop 0
	global_load_dwordx4 v[14:17], v[14:15], off offset:3072
	v_add_co_u32_e32 v162, vcc, 0x1000, v160
	s_nop 1
	v_addc_co_u32_e32 v163, vcc, 0, v161, vcc
	global_load_dwordx4 v[112:115], v[162:163], off
	global_load_dwordx4 v[116:119], v[162:163], off offset:1024
	global_load_dwordx4 v[120:123], v[162:163], off offset:2048
	global_load_dwordx4 v[124:127], v[162:163], off offset:3072
	v_add_co_u32_e32 v164, vcc, 0x2000, v160
	s_nop 1
	v_addc_co_u32_e32 v165, vcc, 0, v161, vcc
	global_load_dwordx4 v[128:131], v[164:165], off
	global_load_dwordx4 v[132:135], v[164:165], off offset:1024
	global_load_dwordx4 v[136:139], v[164:165], off offset:2048
	global_load_dwordx4 v[140:143], v[164:165], off offset:3072
	v_add_co_u32_e32 v166, vcc, 0x3000, v160
	s_nop 1
	v_addc_co_u32_e32 v167, vcc, 0, v161, vcc
	global_load_dwordx4 v[144:147], v[166:167], off
	global_load_dwordx4 v[148:151], v[166:167], off offset:1024
	global_load_dwordx4 v[152:155], v[166:167], off offset:2048
	global_load_dwordx4 v[156:159], v[166:167], off offset:3072
	s_waitcnt vmcnt(15)
	v_lshlrev_b32_e32 v1, 16, v2
	v_and_b32_e32 v2, 0xffff0000, v2
	v_mul_f32_e32 v2, v2, v2
	v_lshlrev_b32_e32 v18, 16, v3
	v_fmac_f32_e32 v2, v1, v1
	v_and_b32_e32 v3, 0xffff0000, v3
	v_fmac_f32_e32 v2, v18, v18
	v_lshlrev_b32_e32 v19, 16, v4
	v_fmac_f32_e32 v2, v3, v3
	v_and_b32_e32 v4, 0xffff0000, v4
	v_fmac_f32_e32 v2, v19, v19
	v_lshlrev_b32_e32 v20, 16, v5
	v_fmac_f32_e32 v2, v4, v4
	v_and_b32_e32 v5, 0xffff0000, v5
	v_fmac_f32_e32 v2, v20, v20
	s_waitcnt vmcnt(14)
	v_lshlrev_b32_e32 v21, 16, v6
	v_fmac_f32_e32 v2, v5, v5
	v_and_b32_e32 v6, 0xffff0000, v6
	v_fmac_f32_e32 v2, v21, v21
	v_lshlrev_b32_e32 v22, 16, v7
	v_fmac_f32_e32 v2, v6, v6
	v_and_b32_e32 v7, 0xffff0000, v7
	v_fmac_f32_e32 v2, v22, v22
	v_lshlrev_b32_e32 v23, 16, v8
	v_fmac_f32_e32 v2, v7, v7
	v_and_b32_e32 v8, 0xffff0000, v8
	v_fmac_f32_e32 v2, v23, v23
	v_lshlrev_b32_e32 v24, 16, v9
	v_fmac_f32_e32 v2, v8, v8
	v_and_b32_e32 v9, 0xffff0000, v9
	v_fmac_f32_e32 v2, v24, v24
	s_waitcnt vmcnt(13)
	v_lshlrev_b32_e32 v25, 16, v10
	v_fmac_f32_e32 v2, v9, v9
	v_and_b32_e32 v10, 0xffff0000, v10
	v_fmac_f32_e32 v2, v25, v25
	v_lshlrev_b32_e32 v26, 16, v11
	v_fmac_f32_e32 v2, v10, v10
	v_and_b32_e32 v11, 0xffff0000, v11
	v_fmac_f32_e32 v2, v26, v26
	v_lshlrev_b32_e32 v27, 16, v12
	v_fmac_f32_e32 v2, v11, v11
	v_and_b32_e32 v12, 0xffff0000, v12
	v_fmac_f32_e32 v2, v27, v27
	v_lshlrev_b32_e32 v28, 16, v13
	v_fmac_f32_e32 v2, v12, v12
	v_and_b32_e32 v13, 0xffff0000, v13
	v_fmac_f32_e32 v2, v28, v28
	s_waitcnt vmcnt(12)
	v_lshlrev_b32_e32 v29, 16, v14
	v_fmac_f32_e32 v2, v13, v13
	v_and_b32_e32 v14, 0xffff0000, v14
	v_fmac_f32_e32 v2, v29, v29
	v_lshlrev_b32_e32 v30, 16, v15
	v_fmac_f32_e32 v2, v14, v14
	v_and_b32_e32 v15, 0xffff0000, v15
	v_fmac_f32_e32 v2, v30, v30
	v_lshlrev_b32_e32 v31, 16, v16
	v_fmac_f32_e32 v2, v15, v15
	v_and_b32_e32 v16, 0xffff0000, v16
	v_fmac_f32_e32 v2, v31, v31
	v_lshlrev_b32_e32 v32, 16, v17
	v_fmac_f32_e32 v2, v16, v16
	v_and_b32_e32 v1, 0xffff0000, v17
	v_fmac_f32_e32 v2, v32, v32
	v_fmac_f32_e32 v2, v1, v1
	s_waitcnt lgkmcnt(0)
	s_nop 1
	v_add_f32_dpp v1, v2, v2 quad_perm:[1,0,3,2] row_mask:0xf bank_mask:0xf
	s_waitcnt lgkmcnt(0)
	s_nop 1
	v_add_f32_dpp v1, v1, v1 quad_perm:[2,3,0,1] row_mask:0xf bank_mask:0xf
	s_waitcnt lgkmcnt(0)
	s_nop 1
	v_add_f32_dpp v1, v1, v1 row_half_mirror row_mask:0xf bank_mask:0xf
	s_waitcnt lgkmcnt(0)
	s_nop 1
	v_add_f32_dpp v1, v1, v1 row_mirror row_mask:0xf bank_mask:0xf
	s_waitcnt lgkmcnt(0)
	v_mov_b32_e32 v2, v1
	s_nop 1
	v_permlane16_swap_b32_e32 v2, v1
	v_add_f32_e32 v2, v1, v2
	ds_bpermute_b32 v3, v81, v2
	s_and_saveexec_b64 s[36:37], s[2:3]
	s_cbranch_execz .LBB0_1877
	s_waitcnt lgkmcnt(0)
	v_add_f32_e32 v1, v2, v3
	v_fmamk_f32 v1, v1, 0x3a000000, v105
	v_mul_f32_e32 v2, 0x4f800000, v1
	v_cmp_gt_f32_e32 vcc, s81, v1
	s_nop 1
	v_cndmask_b32_e32 v1, v1, v2, vcc
	v_sqrt_f32_e32 v2, v1
	s_nop 0
	v_add_u32_e32 v3, -1, v2
	v_fma_f32 v5, -v3, v2, v1
	v_add_u32_e32 v4, 1, v2
	v_cmp_ge_f32_e64 s[34:35], 0, v5
	s_nop 1
	v_cndmask_b32_e64 v3, v2, v3, s[34:35]
	v_fma_f32 v2, -v4, v2, v1
	v_cmp_lt_f32_e64 s[34:35], 0, v2
	s_nop 1
	v_cndmask_b32_e64 v2, v3, v4, s[34:35]
	v_mul_f32_e32 v3, 0x37800000, v2
	v_cndmask_b32_e32 v2, v2, v3, vcc
	v_cmp_class_f32_e32 vcc, v1, v106
	s_nop 1
	v_cndmask_b32_e32 v1, v2, v1, vcc
	v_div_scale_f32 v2, s[34:35], v1, v1, 1.0
	v_rcp_f32_e32 v3, v2
	s_nop 0
	v_fma_f32 v4, -v2, v3, 1.0
	v_fmac_f32_e32 v3, v4, v3
	v_div_scale_f32 v4, vcc, 1.0, v1, 1.0
	v_mul_f32_e32 v5, v4, v3
	v_fma_f32 v6, -v2, v5, v4
	v_fmac_f32_e32 v5, v6, v3
	v_fma_f32 v2, -v2, v5, v4
	v_div_fmas_f32 v2, v2, v3, v5
	v_div_fixup_f32 v1, v2, v1, 1.0
	v_mov_b32_e32 v2, s68
	ds_write_b32 v2, v1
.LBB0_1877:
	s_or_b64 exec, exec, s[36:37]
	s_or_b32 s34, s60, 1
	s_ashr_i32 s35, s34, 31
	s_lshl_b64 s[34:35], s[34:35], 12
	s_waitcnt lgkmcnt(0)
	s_waitcnt vmcnt(8)
	v_mov_b32_e32 v2, v112
	v_mov_b32_e32 v3, v113
	v_mov_b32_e32 v4, v114
	v_mov_b32_e32 v5, v115
	v_mov_b32_e32 v6, v116
	v_mov_b32_e32 v7, v117
	v_mov_b32_e32 v8, v118
	v_mov_b32_e32 v9, v119
	v_mov_b32_e32 v10, v120
	v_mov_b32_e32 v11, v121
	v_mov_b32_e32 v12, v122
	v_mov_b32_e32 v13, v123
	v_mov_b32_e32 v14, v124
	v_mov_b32_e32 v15, v125
	v_mov_b32_e32 v16, v126
	v_mov_b32_e32 v17, v127
	s_nop 0
	v_lshlrev_b32_e32 v1, 16, v2
	v_and_b32_e32 v2, 0xffff0000, v2
	v_mul_f32_e32 v2, v2, v2
	v_lshlrev_b32_e32 v18, 16, v3
	v_fmac_f32_e32 v2, v1, v1
	v_and_b32_e32 v3, 0xffff0000, v3
	v_fmac_f32_e32 v2, v18, v18
	v_lshlrev_b32_e32 v19, 16, v4
	v_fmac_f32_e32 v2, v3, v3
	v_and_b32_e32 v4, 0xffff0000, v4
	v_fmac_f32_e32 v2, v19, v19
	v_lshlrev_b32_e32 v20, 16, v5
	v_fmac_f32_e32 v2, v4, v4
	v_and_b32_e32 v5, 0xffff0000, v5
	v_fmac_f32_e32 v2, v20, v20
	v_lshlrev_b32_e32 v21, 16, v6
	v_fmac_f32_e32 v2, v5, v5
	v_and_b32_e32 v6, 0xffff0000, v6
	v_fmac_f32_e32 v2, v21, v21
	v_lshlrev_b32_e32 v22, 16, v7
	v_fmac_f32_e32 v2, v6, v6
	v_and_b32_e32 v7, 0xffff0000, v7
	v_fmac_f32_e32 v2, v22, v22
	v_lshlrev_b32_e32 v23, 16, v8
	v_fmac_f32_e32 v2, v7, v7
	v_and_b32_e32 v8, 0xffff0000, v8
	v_fmac_f32_e32 v2, v23, v23
	v_lshlrev_b32_e32 v24, 16, v9
	v_fmac_f32_e32 v2, v8, v8
	v_and_b32_e32 v9, 0xffff0000, v9
	v_fmac_f32_e32 v2, v24, v24
	v_lshlrev_b32_e32 v25, 16, v10
	v_fmac_f32_e32 v2, v9, v9
	v_and_b32_e32 v10, 0xffff0000, v10
	v_fmac_f32_e32 v2, v25, v25
	v_lshlrev_b32_e32 v26, 16, v11
	v_fmac_f32_e32 v2, v10, v10
	v_and_b32_e32 v11, 0xffff0000, v11
	v_fmac_f32_e32 v2, v26, v26
	v_lshlrev_b32_e32 v27, 16, v12
	v_fmac_f32_e32 v2, v11, v11
	v_and_b32_e32 v12, 0xffff0000, v12
	v_fmac_f32_e32 v2, v27, v27
	v_lshlrev_b32_e32 v28, 16, v13
	v_fmac_f32_e32 v2, v12, v12
	v_and_b32_e32 v13, 0xffff0000, v13
	v_fmac_f32_e32 v2, v28, v28
	v_lshlrev_b32_e32 v29, 16, v14
	v_fmac_f32_e32 v2, v13, v13
	v_and_b32_e32 v14, 0xffff0000, v14
	v_fmac_f32_e32 v2, v29, v29
	v_lshlrev_b32_e32 v30, 16, v15
	v_fmac_f32_e32 v2, v14, v14
	v_and_b32_e32 v15, 0xffff0000, v15
	v_fmac_f32_e32 v2, v30, v30
	v_lshlrev_b32_e32 v31, 16, v16
	v_fmac_f32_e32 v2, v15, v15
	v_and_b32_e32 v16, 0xffff0000, v16
	v_fmac_f32_e32 v2, v31, v31
	v_lshlrev_b32_e32 v32, 16, v17
	v_fmac_f32_e32 v2, v16, v16
	v_and_b32_e32 v1, 0xffff0000, v17
	v_fmac_f32_e32 v2, v32, v32
	v_fmac_f32_e32 v2, v1, v1
	s_waitcnt lgkmcnt(0)
	s_nop 1
	v_add_f32_dpp v1, v2, v2 quad_perm:[1,0,3,2] row_mask:0xf bank_mask:0xf
	s_waitcnt lgkmcnt(0)
	s_nop 1
	v_add_f32_dpp v1, v1, v1 quad_perm:[2,3,0,1] row_mask:0xf bank_mask:0xf
	s_waitcnt lgkmcnt(0)
	s_nop 1
	v_add_f32_dpp v1, v1, v1 row_half_mirror row_mask:0xf bank_mask:0xf
	s_waitcnt lgkmcnt(0)
	s_nop 1
	v_add_f32_dpp v1, v1, v1 row_mirror row_mask:0xf bank_mask:0xf
	s_waitcnt lgkmcnt(0)
	v_mov_b32_e32 v2, v1
	s_nop 1
	v_permlane16_swap_b32_e32 v2, v1
	v_add_f32_e32 v2, v1, v2
	ds_bpermute_b32 v3, v81, v2
	s_and_saveexec_b64 s[36:37], s[2:3]
	s_cbranch_execz .LBB0_1879
	s_waitcnt lgkmcnt(0)
	v_add_f32_e32 v1, v2, v3
	v_fmamk_f32 v1, v1, 0x3a000000, v105
	v_mul_f32_e32 v2, 0x4f800000, v1
	v_cmp_gt_f32_e32 vcc, s81, v1
	s_nop 1
	v_cndmask_b32_e32 v1, v1, v2, vcc
	v_sqrt_f32_e32 v2, v1
	s_nop 0
	v_add_u32_e32 v3, -1, v2
	v_fma_f32 v5, -v3, v2, v1
	v_add_u32_e32 v4, 1, v2
	v_cmp_ge_f32_e64 s[34:35], 0, v5
	s_nop 1
	v_cndmask_b32_e64 v3, v2, v3, s[34:35]
	v_fma_f32 v2, -v4, v2, v1
	v_cmp_lt_f32_e64 s[34:35], 0, v2
	s_nop 1
	v_cndmask_b32_e64 v2, v3, v4, s[34:35]
	v_mul_f32_e32 v3, 0x37800000, v2
	v_cndmask_b32_e32 v2, v2, v3, vcc
	v_cmp_class_f32_e32 vcc, v1, v106
	s_nop 1
	v_cndmask_b32_e32 v1, v2, v1, vcc
	v_div_scale_f32 v2, s[34:35], v1, v1, 1.0
	v_rcp_f32_e32 v3, v2
	s_nop 0
	v_fma_f32 v4, -v2, v3, 1.0
	v_fmac_f32_e32 v3, v4, v3
	v_div_scale_f32 v4, vcc, 1.0, v1, 1.0
	v_mul_f32_e32 v5, v4, v3
	v_fma_f32 v6, -v2, v5, v4
	v_fmac_f32_e32 v5, v6, v3
	v_fma_f32 v2, -v2, v5, v4
	v_div_fmas_f32 v2, v2, v3, v5
	v_div_fixup_f32 v1, v2, v1, 1.0
	v_mov_b32_e32 v2, s68
	ds_write_b32 v2, v1 offset:4
.LBB0_1879:
	s_or_b64 exec, exec, s[36:37]
	s_or_b32 s34, s60, 2
	s_ashr_i32 s35, s34, 31
	s_lshl_b64 s[34:35], s[34:35], 12
	s_waitcnt lgkmcnt(0)
	s_waitcnt vmcnt(4)
	v_mov_b32_e32 v2, v128
	v_mov_b32_e32 v3, v129
	v_mov_b32_e32 v4, v130
	v_mov_b32_e32 v5, v131
	v_mov_b32_e32 v6, v132
	v_mov_b32_e32 v7, v133
	v_mov_b32_e32 v8, v134
	v_mov_b32_e32 v9, v135
	v_mov_b32_e32 v10, v136
	v_mov_b32_e32 v11, v137
	v_mov_b32_e32 v12, v138
	v_mov_b32_e32 v13, v139
	v_mov_b32_e32 v14, v140
	v_mov_b32_e32 v15, v141
	v_mov_b32_e32 v16, v142
	v_mov_b32_e32 v17, v143
	s_nop 0
	v_lshlrev_b32_e32 v1, 16, v2
	v_and_b32_e32 v2, 0xffff0000, v2
	v_mul_f32_e32 v2, v2, v2
	v_lshlrev_b32_e32 v18, 16, v3
	v_fmac_f32_e32 v2, v1, v1
	v_and_b32_e32 v3, 0xffff0000, v3
	v_fmac_f32_e32 v2, v18, v18
	v_lshlrev_b32_e32 v19, 16, v4
	v_fmac_f32_e32 v2, v3, v3
	v_and_b32_e32 v4, 0xffff0000, v4
	v_fmac_f32_e32 v2, v19, v19
	v_lshlrev_b32_e32 v20, 16, v5
	v_fmac_f32_e32 v2, v4, v4
	v_and_b32_e32 v5, 0xffff0000, v5
	v_fmac_f32_e32 v2, v20, v20
	v_lshlrev_b32_e32 v21, 16, v6
	v_fmac_f32_e32 v2, v5, v5
	v_and_b32_e32 v6, 0xffff0000, v6
	v_fmac_f32_e32 v2, v21, v21
	v_lshlrev_b32_e32 v22, 16, v7
	v_fmac_f32_e32 v2, v6, v6
	v_and_b32_e32 v7, 0xffff0000, v7
	v_fmac_f32_e32 v2, v22, v22
	v_lshlrev_b32_e32 v23, 16, v8
	v_fmac_f32_e32 v2, v7, v7
	v_and_b32_e32 v8, 0xffff0000, v8
	v_fmac_f32_e32 v2, v23, v23
	v_lshlrev_b32_e32 v24, 16, v9
	v_fmac_f32_e32 v2, v8, v8
	v_and_b32_e32 v9, 0xffff0000, v9
	v_fmac_f32_e32 v2, v24, v24
	v_lshlrev_b32_e32 v25, 16, v10
	v_fmac_f32_e32 v2, v9, v9
	v_and_b32_e32 v10, 0xffff0000, v10
	v_fmac_f32_e32 v2, v25, v25
	v_lshlrev_b32_e32 v26, 16, v11
	v_fmac_f32_e32 v2, v10, v10
	v_and_b32_e32 v11, 0xffff0000, v11
	v_fmac_f32_e32 v2, v26, v26
	v_lshlrev_b32_e32 v27, 16, v12
	v_fmac_f32_e32 v2, v11, v11
	v_and_b32_e32 v12, 0xffff0000, v12
	v_fmac_f32_e32 v2, v27, v27
	v_lshlrev_b32_e32 v28, 16, v13
	v_fmac_f32_e32 v2, v12, v12
	v_and_b32_e32 v13, 0xffff0000, v13
	v_fmac_f32_e32 v2, v28, v28
	v_lshlrev_b32_e32 v29, 16, v14
	v_fmac_f32_e32 v2, v13, v13
	v_and_b32_e32 v14, 0xffff0000, v14
	v_fmac_f32_e32 v2, v29, v29
	v_lshlrev_b32_e32 v30, 16, v15
	v_fmac_f32_e32 v2, v14, v14
	v_and_b32_e32 v15, 0xffff0000, v15
	v_fmac_f32_e32 v2, v30, v30
	v_lshlrev_b32_e32 v31, 16, v16
	v_fmac_f32_e32 v2, v15, v15
	v_and_b32_e32 v16, 0xffff0000, v16
	v_fmac_f32_e32 v2, v31, v31
	v_lshlrev_b32_e32 v32, 16, v17
	v_fmac_f32_e32 v2, v16, v16
	v_and_b32_e32 v1, 0xffff0000, v17
	v_fmac_f32_e32 v2, v32, v32
	v_fmac_f32_e32 v2, v1, v1
	s_waitcnt lgkmcnt(0)
	s_nop 1
	v_add_f32_dpp v1, v2, v2 quad_perm:[1,0,3,2] row_mask:0xf bank_mask:0xf
	s_waitcnt lgkmcnt(0)
	s_nop 1
	v_add_f32_dpp v1, v1, v1 quad_perm:[2,3,0,1] row_mask:0xf bank_mask:0xf
	s_waitcnt lgkmcnt(0)
	s_nop 1
	v_add_f32_dpp v1, v1, v1 row_half_mirror row_mask:0xf bank_mask:0xf
	s_waitcnt lgkmcnt(0)
	s_nop 1
	v_add_f32_dpp v1, v1, v1 row_mirror row_mask:0xf bank_mask:0xf
	s_waitcnt lgkmcnt(0)
	v_mov_b32_e32 v2, v1
	s_nop 1
	v_permlane16_swap_b32_e32 v2, v1
	v_add_f32_e32 v2, v1, v2
	ds_bpermute_b32 v3, v81, v2
	s_and_saveexec_b64 s[36:37], s[2:3]
	s_cbranch_execz .LBB0_1881
	s_waitcnt lgkmcnt(0)
	v_add_f32_e32 v1, v2, v3
	v_fmamk_f32 v1, v1, 0x3a000000, v105
	v_mul_f32_e32 v2, 0x4f800000, v1
	v_cmp_gt_f32_e32 vcc, s81, v1
	s_nop 1
	v_cndmask_b32_e32 v1, v1, v2, vcc
	v_sqrt_f32_e32 v2, v1
	s_nop 0
	v_add_u32_e32 v3, -1, v2
	v_fma_f32 v5, -v3, v2, v1
	v_add_u32_e32 v4, 1, v2
	v_cmp_ge_f32_e64 s[34:35], 0, v5
	s_nop 1
	v_cndmask_b32_e64 v3, v2, v3, s[34:35]
	v_fma_f32 v2, -v4, v2, v1
	v_cmp_lt_f32_e64 s[34:35], 0, v2
	s_nop 1
	v_cndmask_b32_e64 v2, v3, v4, s[34:35]
	v_mul_f32_e32 v3, 0x37800000, v2
	v_cndmask_b32_e32 v2, v2, v3, vcc
	v_cmp_class_f32_e32 vcc, v1, v106
	s_nop 1
	v_cndmask_b32_e32 v1, v2, v1, vcc
	v_div_scale_f32 v2, s[34:35], v1, v1, 1.0
	v_rcp_f32_e32 v3, v2
	s_nop 0
	v_fma_f32 v4, -v2, v3, 1.0
	v_fmac_f32_e32 v3, v4, v3
	v_div_scale_f32 v4, vcc, 1.0, v1, 1.0
	v_mul_f32_e32 v5, v4, v3
	v_fma_f32 v6, -v2, v5, v4
	v_fmac_f32_e32 v5, v6, v3
	v_fma_f32 v2, -v2, v5, v4
	v_div_fmas_f32 v2, v2, v3, v5
	v_div_fixup_f32 v1, v2, v1, 1.0
	v_mov_b32_e32 v2, s68
	ds_write_b32 v2, v1 offset:8
.LBB0_1881:
	s_or_b64 exec, exec, s[36:37]
	s_or_b32 s34, s60, 3
	s_ashr_i32 s35, s34, 31
	s_lshl_b64 s[34:35], s[34:35], 12
	s_waitcnt lgkmcnt(0)
	s_waitcnt vmcnt(0)
	v_mov_b32_e32 v2, v144
	v_mov_b32_e32 v3, v145
	v_mov_b32_e32 v4, v146
	v_mov_b32_e32 v5, v147
	v_mov_b32_e32 v6, v148
	v_mov_b32_e32 v7, v149
	v_mov_b32_e32 v8, v150
	v_mov_b32_e32 v9, v151
	v_mov_b32_e32 v10, v152
	v_mov_b32_e32 v11, v153
	v_mov_b32_e32 v12, v154
	v_mov_b32_e32 v13, v155
	v_mov_b32_e32 v14, v156
	v_mov_b32_e32 v15, v157
	v_mov_b32_e32 v16, v158
	v_mov_b32_e32 v17, v159
	s_nop 0
	v_lshlrev_b32_e32 v1, 16, v2
	v_and_b32_e32 v2, 0xffff0000, v2
	v_mul_f32_e32 v2, v2, v2
	v_lshlrev_b32_e32 v18, 16, v3
	v_fmac_f32_e32 v2, v1, v1
	v_and_b32_e32 v3, 0xffff0000, v3
	v_fmac_f32_e32 v2, v18, v18
	v_lshlrev_b32_e32 v19, 16, v4
	v_fmac_f32_e32 v2, v3, v3
	v_and_b32_e32 v4, 0xffff0000, v4
	v_fmac_f32_e32 v2, v19, v19
	v_lshlrev_b32_e32 v20, 16, v5
	v_fmac_f32_e32 v2, v4, v4
	v_and_b32_e32 v5, 0xffff0000, v5
	v_fmac_f32_e32 v2, v20, v20
	v_lshlrev_b32_e32 v21, 16, v6
	v_fmac_f32_e32 v2, v5, v5
	v_and_b32_e32 v6, 0xffff0000, v6
	v_fmac_f32_e32 v2, v21, v21
	v_lshlrev_b32_e32 v22, 16, v7
	v_fmac_f32_e32 v2, v6, v6
	v_and_b32_e32 v7, 0xffff0000, v7
	v_fmac_f32_e32 v2, v22, v22
	v_lshlrev_b32_e32 v23, 16, v8
	v_fmac_f32_e32 v2, v7, v7
	v_and_b32_e32 v8, 0xffff0000, v8
	v_fmac_f32_e32 v2, v23, v23
	v_lshlrev_b32_e32 v24, 16, v9
	v_fmac_f32_e32 v2, v8, v8
	v_and_b32_e32 v9, 0xffff0000, v9
	v_fmac_f32_e32 v2, v24, v24
	v_lshlrev_b32_e32 v25, 16, v10
	v_fmac_f32_e32 v2, v9, v9
	v_and_b32_e32 v10, 0xffff0000, v10
	v_fmac_f32_e32 v2, v25, v25
	v_lshlrev_b32_e32 v26, 16, v11
	v_fmac_f32_e32 v2, v10, v10
	v_and_b32_e32 v11, 0xffff0000, v11
	v_fmac_f32_e32 v2, v26, v26
	v_lshlrev_b32_e32 v27, 16, v12
	v_fmac_f32_e32 v2, v11, v11
	v_and_b32_e32 v12, 0xffff0000, v12
	v_fmac_f32_e32 v2, v27, v27
	v_lshlrev_b32_e32 v28, 16, v13
	v_fmac_f32_e32 v2, v12, v12
	v_and_b32_e32 v13, 0xffff0000, v13
	v_fmac_f32_e32 v2, v28, v28
	v_lshlrev_b32_e32 v29, 16, v14
	v_fmac_f32_e32 v2, v13, v13
	v_and_b32_e32 v14, 0xffff0000, v14
	v_fmac_f32_e32 v2, v29, v29
	v_lshlrev_b32_e32 v30, 16, v15
	v_fmac_f32_e32 v2, v14, v14
	v_and_b32_e32 v15, 0xffff0000, v15
	v_fmac_f32_e32 v2, v30, v30
	v_lshlrev_b32_e32 v31, 16, v16
	v_fmac_f32_e32 v2, v15, v15
	v_and_b32_e32 v16, 0xffff0000, v16
	v_fmac_f32_e32 v2, v31, v31
	v_lshlrev_b32_e32 v32, 16, v17
	v_fmac_f32_e32 v2, v16, v16
	v_and_b32_e32 v1, 0xffff0000, v17
	v_fmac_f32_e32 v2, v32, v32
	v_fmac_f32_e32 v2, v1, v1
	s_waitcnt lgkmcnt(0)
	s_nop 1
	v_add_f32_dpp v1, v2, v2 quad_perm:[1,0,3,2] row_mask:0xf bank_mask:0xf
	s_waitcnt lgkmcnt(0)
	s_nop 1
	v_add_f32_dpp v1, v1, v1 quad_perm:[2,3,0,1] row_mask:0xf bank_mask:0xf
	s_waitcnt lgkmcnt(0)
	s_nop 1
	v_add_f32_dpp v1, v1, v1 row_half_mirror row_mask:0xf bank_mask:0xf
	s_waitcnt lgkmcnt(0)
	s_nop 1
	v_add_f32_dpp v1, v1, v1 row_mirror row_mask:0xf bank_mask:0xf
	s_waitcnt lgkmcnt(0)
	v_mov_b32_e32 v2, v1
	s_nop 1
	v_permlane16_swap_b32_e32 v2, v1
	v_add_f32_e32 v2, v1, v2
	ds_bpermute_b32 v3, v81, v2
	s_and_saveexec_b64 s[36:37], s[2:3]
	s_cbranch_execz .LBB0_1883
	s_waitcnt lgkmcnt(0)
	v_add_f32_e32 v1, v2, v3
	v_fmamk_f32 v1, v1, 0x3a000000, v105
	v_mul_f32_e32 v2, 0x4f800000, v1
	v_cmp_gt_f32_e32 vcc, s81, v1
	s_nop 1
	v_cndmask_b32_e32 v1, v1, v2, vcc
	v_sqrt_f32_e32 v2, v1
	s_nop 0
	v_add_u32_e32 v3, -1, v2
	v_fma_f32 v5, -v3, v2, v1
	v_add_u32_e32 v4, 1, v2
	v_cmp_ge_f32_e64 s[34:35], 0, v5
	s_nop 1
	v_cndmask_b32_e64 v3, v2, v3, s[34:35]
	v_fma_f32 v2, -v4, v2, v1
	v_cmp_lt_f32_e64 s[34:35], 0, v2
	s_nop 1
	v_cndmask_b32_e64 v2, v3, v4, s[34:35]
	v_mul_f32_e32 v3, 0x37800000, v2
	v_cndmask_b32_e32 v2, v2, v3, vcc
	v_cmp_class_f32_e32 vcc, v1, v106
	s_nop 1
	v_cndmask_b32_e32 v1, v2, v1, vcc
	v_div_scale_f32 v2, s[34:35], v1, v1, 1.0
	v_rcp_f32_e32 v3, v2
	s_nop 0
	v_fma_f32 v4, -v2, v3, 1.0
	v_fmac_f32_e32 v3, v4, v3
	v_div_scale_f32 v4, vcc, 1.0, v1, 1.0
	v_mul_f32_e32 v5, v4, v3
	v_fma_f32 v6, -v2, v5, v4
	v_fmac_f32_e32 v5, v6, v3
	v_fma_f32 v2, -v2, v5, v4
	v_div_fmas_f32 v2, v2, v3, v5
	v_div_fixup_f32 v1, v2, v1, 1.0
	v_mov_b32_e32 v2, s68
	ds_write_b32 v2, v1 offset:12

.LBB0_1884:
	v_and_b32_e32 v62, 0xffffff00, v103
	v_lshl_add_u32 v63, v254, 2, v62
	v_lshlrev_b32_e32 v63, 2, v63
	global_load_dwordx4 v[200:203], v63, s[62:63]
	global_load_dwordx4 v[204:207], v63, s[34:35]
	global_load_dwordx4 v[208:211], v63, s[36:37]
	v_lshlrev_b32_e32 v64, 1, v103
	v_mov_b32_e32 v65, 0
	v_mov_b32_e32 v66, v103
	v_mov_b32_e32 v67, 0
	v_lshl_add_u64 v[196:197], v[48:49], 0, v[64:65]
	v_lshlrev_b32_e32 v68, 6, v62
	v_lshl_add_u32 v68, v254, 4, v68
	v_lshlrev_b32_e32 v69, 12, v75
	v_sub_u32_e32 v68, v68, v69
	v_ashrrev_i32_e32 v69, 31, v68
	v_lshl_add_u64 v[34:35], v[34:35], 0, v[68:69]
	v_lshl_add_u64 v[36:37], v[36:37], 0, v[68:69]
	v_lshl_add_u64 v[38:39], v[38:39], 0, v[68:69]
	v_lshl_add_u64 v[40:41], v[40:41], 0, v[68:69]
	v_mov_b32_e32 v198, 0x1000
	v_mov_b32_e32 v199, 0
	v_lshl_add_u64 v[72:73], v[50:51], 0, v[66:67]
	global_load_dwordx4 v[112:115], v[196:197], off
	global_load_dwordx4 v[116:119], v[34:35], off
	global_load_dwordx4 v[120:123], v[36:37], off
	global_load_dwordx4 v[124:127], v[38:39], off
	global_load_dwordx4 v[128:131], v[40:41], off
	global_load_dwordx4 v[132:135], v[196:197], off offset:32
	global_load_dwordx4 v[136:139], v[34:35], off offset:1024
	global_load_dwordx4 v[140:143], v[36:37], off offset:1024
	global_load_dwordx4 v[144:147], v[38:39], off offset:1024
	global_load_dwordx4 v[148:151], v[40:41], off offset:1024
	global_load_dwordx4 v[152:155], v[196:197], off offset:64
	global_load_dwordx4 v[156:159], v[34:35], off offset:2048
	global_load_dwordx4 v[160:163], v[36:37], off offset:2048
	global_load_dwordx4 v[164:167], v[38:39], off offset:2048
	global_load_dwordx4 v[168:171], v[40:41], off offset:2048
	global_load_dwordx4 v[172:175], v[196:197], off offset:96
	global_load_dwordx4 v[176:179], v[34:35], off offset:3072
	global_load_dwordx4 v[180:183], v[36:37], off offset:3072
	global_load_dwordx4 v[184:187], v[38:39], off offset:3072
	global_load_dwordx4 v[188:191], v[40:41], off offset:3072
	v_mul_u32_u24_e32 v62, 12, v62
	v_add_u32_e32 v62, 0x12000, v62
	v_lshl_add_u32 v1, v254, 4, v62
	v_and_b32_e32 v63, 8, v103
	v_lshl_add_u32 v111, v63, 2, v62
	s_waitcnt vmcnt(20)
	v_pk_add_f32 v[204:205], v[204:205], 1.0 op_sel_hi:[1,0]
	v_pk_add_f32 v[206:207], v[206:207], 1.0 op_sel_hi:[1,0]
	ds_write_b128 v1, v[200:203]
	ds_write_b128 v1, v[204:207] offset:1024
	ds_write_b128 v1, v[208:211] offset:2048
	s_waitcnt lgkmcnt(0)
	ds_read_b128 v[200:203], v111 offset:0
	ds_read_b128 v[204:207], v111 offset:16
	ds_read_b128 v[208:211], v111 offset:1024
	ds_read_b128 v[212:215], v111 offset:1040
	ds_read_b128 v[216:219], v111 offset:2048
	ds_read_b128 v[220:223], v111 offset:2064
	s_waitcnt lgkmcnt(0)
	ds_read_b128 v[224:227], v111 offset:64
	ds_read_b128 v[228:231], v111 offset:80
	ds_read_b128 v[232:235], v111 offset:1088
	ds_read_b128 v[236:239], v111 offset:1104
	ds_read_b128 v[240:243], v111 offset:2112
	ds_read_b128 v[244:247], v111 offset:2128
	s_waitcnt vmcnt(15)
	v_lshlrev_b32_e32 v54, 16, v112
	v_and_b32_e32 v55, 0xffff0000, v112
	v_lshlrev_b32_e32 v56, 16, v113
	v_and_b32_e32 v57, 0xffff0000, v113
	v_lshlrev_b32_e32 v58, 16, v114
	v_and_b32_e32 v59, 0xffff0000, v114
	v_lshlrev_b32_e32 v60, 16, v115
	v_and_b32_e32 v61, 0xffff0000, v115
	v_pk_mul_f32 v[54:55], v[46:47], v[54:55]
	v_pk_mul_f32 v[56:57], v[46:47], v[56:57]
	v_pk_mul_f32 v[58:59], v[46:47], v[58:59]
	v_pk_mul_f32 v[60:61], v[46:47], v[60:61]
	v_pk_mul_f32 v[54:55], v[200:201], v[54:55]
	v_pk_mul_f32 v[56:57], v[202:203], v[56:57]
	v_pk_mul_f32 v[58:59], v[204:205], v[58:59]
	v_pk_mul_f32 v[60:61], v[206:207], v[60:61]
	v_pk_fma_f32 v[54:55], v[208:209], v[54:55], v[216:217]
	v_pk_fma_f32 v[56:57], v[210:211], v[56:57], v[218:219]
	v_pk_fma_f32 v[58:59], v[212:213], v[58:59], v[220:221]
	v_pk_fma_f32 v[60:61], v[214:215], v[60:61], v[222:223]
	v_med3_f32 v62, v54, s82, v108
	v_med3_f32 v63, v55, s82, v108
	v_med3_f32 v64, v56, s82, v108
	v_med3_f32 v65, v57, s82, v108
	v_med3_f32 v66, v58, s82, v108
	v_med3_f32 v67, v59, s82, v108
	v_med3_f32 v68, v60, s82, v108
	v_med3_f32 v69, v61, s82, v108
	v_cvt_pk_bf16_f32 v192, v54, v55
	v_cvt_pk_bf16_f32 v193, v56, v57
	v_cvt_pk_bf16_f32 v194, v58, v59
	v_cvt_pk_bf16_f32 v195, v60, v61
	v_cvt_pk_fp8_f32 v70, v62, v63
	v_cvt_pk_fp8_f32 v71, v66, v67
	v_cvt_pk_fp8_f32 v70, v64, v65 op_sel:[0,0,1]
	v_cvt_pk_fp8_f32 v71, v68, v69 op_sel:[0,0,1]
	s_nop 0
	global_store_dwordx2 v[72:73], v[70:71], off
	v_mfma_f32_32x32x16_bf16 v[2:17], v[192:195], v[116:119], v[2:17]
	v_mfma_f32_32x32x16_bf16 v[18:33], v[192:195], v[120:123], v[18:33]
	v_mfma_f32_32x32x16_bf16 v[2:17], v[192:195], v[124:127], v[2:17]
	v_mfma_f32_32x32x16_bf16 v[18:33], v[192:195], v[128:131], v[18:33]
	v_lshlrev_b32_e32 v252, 16, v192
	v_and_b32_e32 v253, 0xffff0000, v192
	v_sub_f32_e32 v62, v54, v252
	v_sub_f32_e32 v63, v55, v253
	v_lshlrev_b32_e32 v252, 16, v193
	v_and_b32_e32 v253, 0xffff0000, v193
	v_sub_f32_e32 v64, v56, v252
	v_sub_f32_e32 v65, v57, v253
	v_lshlrev_b32_e32 v252, 16, v194
	v_and_b32_e32 v253, 0xffff0000, v194
	v_sub_f32_e32 v66, v58, v252
	v_sub_f32_e32 v67, v59, v253
	v_lshlrev_b32_e32 v252, 16, v195
	v_and_b32_e32 v253, 0xffff0000, v195
	v_sub_f32_e32 v68, v60, v252
	v_sub_f32_e32 v69, v61, v253
	v_cvt_pk_bf16_f32 v248, v62, v63
	v_cvt_pk_bf16_f32 v249, v64, v65
	v_cvt_pk_bf16_f32 v250, v66, v67
	v_cvt_pk_bf16_f32 v251, v68, v69
	s_nop 1
	v_mfma_f32_32x32x16_bf16 v[2:17], v[248:251], v[116:119], v[2:17]
	v_mfma_f32_32x32x16_bf16 v[18:33], v[248:251], v[120:123], v[18:33]
	global_load_dwordx4 v[112:115], v[196:197], off offset:128
	v_lshl_add_u64 v[34:35], v[34:35], 0, v[198:199]
	v_lshl_add_u64 v[36:37], v[36:37], 0, v[198:199]
	v_lshl_add_u64 v[38:39], v[38:39], 0, v[198:199]
	v_lshl_add_u64 v[40:41], v[40:41], 0, v[198:199]
	global_load_dwordx4 v[116:119], v[34:35], off
	global_load_dwordx4 v[120:123], v[36:37], off
	global_load_dwordx4 v[124:127], v[38:39], off
	global_load_dwordx4 v[128:131], v[40:41], off
	s_waitcnt lgkmcnt(0)
	ds_read_b128 v[200:203], v111 offset:128
	ds_read_b128 v[204:207], v111 offset:144
	ds_read_b128 v[208:211], v111 offset:1152
	ds_read_b128 v[212:215], v111 offset:1168
	ds_read_b128 v[216:219], v111 offset:2176
	ds_read_b128 v[220:223], v111 offset:2192
	s_waitcnt vmcnt(16)
	v_lshlrev_b32_e32 v54, 16, v132
	v_and_b32_e32 v55, 0xffff0000, v132
	v_lshlrev_b32_e32 v56, 16, v133
	v_and_b32_e32 v57, 0xffff0000, v133
	v_lshlrev_b32_e32 v58, 16, v134
	v_and_b32_e32 v59, 0xffff0000, v134
	v_lshlrev_b32_e32 v60, 16, v135
	v_and_b32_e32 v61, 0xffff0000, v135
	v_pk_mul_f32 v[54:55], v[46:47], v[54:55]
	v_pk_mul_f32 v[56:57], v[46:47], v[56:57]
	v_pk_mul_f32 v[58:59], v[46:47], v[58:59]
	v_pk_mul_f32 v[60:61], v[46:47], v[60:61]
	v_pk_mul_f32 v[54:55], v[224:225], v[54:55]
	v_pk_mul_f32 v[56:57], v[226:227], v[56:57]
	v_pk_mul_f32 v[58:59], v[228:229], v[58:59]
	v_pk_mul_f32 v[60:61], v[230:231], v[60:61]
	v_pk_fma_f32 v[54:55], v[232:233], v[54:55], v[240:241]
	v_pk_fma_f32 v[56:57], v[234:235], v[56:57], v[242:243]
	v_pk_fma_f32 v[58:59], v[236:237], v[58:59], v[244:245]
	v_pk_fma_f32 v[60:61], v[238:239], v[60:61], v[246:247]
	v_med3_f32 v62, v54, s82, v108
	v_med3_f32 v63, v55, s82, v108
	v_med3_f32 v64, v56, s82, v108
	v_med3_f32 v65, v57, s82, v108
	v_med3_f32 v66, v58, s82, v108
	v_med3_f32 v67, v59, s82, v108
	v_med3_f32 v68, v60, s82, v108
	v_med3_f32 v69, v61, s82, v108
	v_cvt_pk_bf16_f32 v192, v54, v55
	v_cvt_pk_bf16_f32 v193, v56, v57
	v_cvt_pk_bf16_f32 v194, v58, v59
	v_cvt_pk_bf16_f32 v195, v60, v61
	v_cvt_pk_fp8_f32 v70, v62, v63
	v_cvt_pk_fp8_f32 v71, v66, v67
	v_cvt_pk_fp8_f32 v70, v64, v65 op_sel:[0,0,1]
	v_cvt_pk_fp8_f32 v71, v68, v69 op_sel:[0,0,1]
	s_nop 0
	global_store_dwordx2 v[72:73], v[70:71], off offset:16
	v_mfma_f32_32x32x16_bf16 v[2:17], v[192:195], v[136:139], v[2:17]
	v_mfma_f32_32x32x16_bf16 v[18:33], v[192:195], v[140:143], v[18:33]
	v_mfma_f32_32x32x16_bf16 v[2:17], v[192:195], v[144:147], v[2:17]
	v_mfma_f32_32x32x16_bf16 v[18:33], v[192:195], v[148:151], v[18:33]
	v_lshlrev_b32_e32 v252, 16, v192
	v_and_b32_e32 v253, 0xffff0000, v192
	v_sub_f32_e32 v62, v54, v252
	v_sub_f32_e32 v63, v55, v253
	v_lshlrev_b32_e32 v252, 16, v193
	v_and_b32_e32 v253, 0xffff0000, v193
	v_sub_f32_e32 v64, v56, v252
	v_sub_f32_e32 v65, v57, v253
	v_lshlrev_b32_e32 v252, 16, v194
	v_and_b32_e32 v253, 0xffff0000, v194
	v_sub_f32_e32 v66, v58, v252
	v_sub_f32_e32 v67, v59, v253
	v_lshlrev_b32_e32 v252, 16, v195
	v_and_b32_e32 v253, 0xffff0000, v195
	v_sub_f32_e32 v68, v60, v252
	v_sub_f32_e32 v69, v61, v253
	v_cvt_pk_bf16_f32 v248, v62, v63
	v_cvt_pk_bf16_f32 v249, v64, v65
	v_cvt_pk_bf16_f32 v250, v66, v67
	v_cvt_pk_bf16_f32 v251, v68, v69
	s_nop 1
	v_mfma_f32_32x32x16_bf16 v[2:17], v[248:251], v[136:139], v[2:17]
	v_mfma_f32_32x32x16_bf16 v[18:33], v[248:251], v[140:143], v[18:33]
	global_load_dwordx4 v[132:135], v[196:197], off offset:160
	global_load_dwordx4 v[136:139], v[34:35], off offset:1024
	global_load_dwordx4 v[140:143], v[36:37], off offset:1024
	global_load_dwordx4 v[144:147], v[38:39], off offset:1024
	global_load_dwordx4 v[148:151], v[40:41], off offset:1024
	s_waitcnt lgkmcnt(0)
	ds_read_b128 v[224:227], v111 offset:192
	ds_read_b128 v[228:231], v111 offset:208
	ds_read_b128 v[232:235], v111 offset:1216
	ds_read_b128 v[236:239], v111 offset:1232
	ds_read_b128 v[240:243], v111 offset:2240
	ds_read_b128 v[244:247], v111 offset:2256
	s_waitcnt vmcnt(17)
	v_lshlrev_b32_e32 v54, 16, v152
	v_and_b32_e32 v55, 0xffff0000, v152
	v_lshlrev_b32_e32 v56, 16, v153
	v_and_b32_e32 v57, 0xffff0000, v153
	v_lshlrev_b32_e32 v58, 16, v154
	v_and_b32_e32 v59, 0xffff0000, v154
	v_lshlrev_b32_e32 v60, 16, v155
	v_and_b32_e32 v61, 0xffff0000, v155
	v_pk_mul_f32 v[54:55], v[46:47], v[54:55]
	v_pk_mul_f32 v[56:57], v[46:47], v[56:57]
	v_pk_mul_f32 v[58:59], v[46:47], v[58:59]
	v_pk_mul_f32 v[60:61], v[46:47], v[60:61]
	v_pk_mul_f32 v[54:55], v[200:201], v[54:55]
	v_pk_mul_f32 v[56:57], v[202:203], v[56:57]
	v_pk_mul_f32 v[58:59], v[204:205], v[58:59]
	v_pk_mul_f32 v[60:61], v[206:207], v[60:61]
	v_pk_fma_f32 v[54:55], v[208:209], v[54:55], v[216:217]
	v_pk_fma_f32 v[56:57], v[210:211], v[56:57], v[218:219]
	v_pk_fma_f32 v[58:59], v[212:213], v[58:59], v[220:221]
	v_pk_fma_f32 v[60:61], v[214:215], v[60:61], v[222:223]
	v_med3_f32 v62, v54, s82, v108
	v_med3_f32 v63, v55, s82, v108
	v_med3_f32 v64, v56, s82, v108
	v_med3_f32 v65, v57, s82, v108
	v_med3_f32 v66, v58, s82, v108
	v_med3_f32 v67, v59, s82, v108
	v_med3_f32 v68, v60, s82, v108
	v_med3_f32 v69, v61, s82, v108
	v_cvt_pk_bf16_f32 v192, v54, v55
	v_cvt_pk_bf16_f32 v193, v56, v57
	v_cvt_pk_bf16_f32 v194, v58, v59
	v_cvt_pk_bf16_f32 v195, v60, v61
	v_cvt_pk_fp8_f32 v70, v62, v63
	v_cvt_pk_fp8_f32 v71, v66, v67
	v_cvt_pk_fp8_f32 v70, v64, v65 op_sel:[0,0,1]
	v_cvt_pk_fp8_f32 v71, v68, v69 op_sel:[0,0,1]
	s_nop 0
	global_store_dwordx2 v[72:73], v[70:71], off offset:32
	v_mfma_f32_32x32x16_bf16 v[2:17], v[192:195], v[156:159], v[2:17]
	v_mfma_f32_32x32x16_bf16 v[18:33], v[192:195], v[160:163], v[18:33]
	v_mfma_f32_32x32x16_bf16 v[2:17], v[192:195], v[164:167], v[2:17]
	v_mfma_f32_32x32x16_bf16 v[18:33], v[192:195], v[168:171], v[18:33]
	v_lshlrev_b32_e32 v252, 16, v192
	v_and_b32_e32 v253, 0xffff0000, v192
	v_sub_f32_e32 v62, v54, v252
	v_sub_f32_e32 v63, v55, v253
	v_lshlrev_b32_e32 v252, 16, v193
	v_and_b32_e32 v253, 0xffff0000, v193
	v_sub_f32_e32 v64, v56, v252
	v_sub_f32_e32 v65, v57, v253
	v_lshlrev_b32_e32 v252, 16, v194
	v_and_b32_e32 v253, 0xffff0000, v194
	v_sub_f32_e32 v66, v58, v252
	v_sub_f32_e32 v67, v59, v253
	v_lshlrev_b32_e32 v252, 16, v195
	v_and_b32_e32 v253, 0xffff0000, v195
	v_sub_f32_e32 v68, v60, v252
	v_sub_f32_e32 v69, v61, v253
	v_cvt_pk_bf16_f32 v248, v62, v63
	v_cvt_pk_bf16_f32 v249, v64, v65
	v_cvt_pk_bf16_f32 v250, v66, v67
	v_cvt_pk_bf16_f32 v251, v68, v69
	s_nop 1
	v_mfma_f32_32x32x16_bf16 v[2:17], v[248:251], v[156:159], v[2:17]
	v_mfma_f32_32x32x16_bf16 v[18:33], v[248:251], v[160:163], v[18:33]
	global_load_dwordx4 v[152:155], v[196:197], off offset:192
	global_load_dwordx4 v[156:159], v[34:35], off offset:2048
	global_load_dwordx4 v[160:163], v[36:37], off offset:2048
	global_load_dwordx4 v[164:167], v[38:39], off offset:2048
	global_load_dwordx4 v[168:171], v[40:41], off offset:2048
	s_waitcnt lgkmcnt(0)
	ds_read_b128 v[200:203], v111 offset:256
	ds_read_b128 v[204:207], v111 offset:272
	ds_read_b128 v[208:211], v111 offset:1280
	ds_read_b128 v[212:215], v111 offset:1296
	ds_read_b128 v[216:219], v111 offset:2304
	ds_read_b128 v[220:223], v111 offset:2320
	s_waitcnt vmcnt(18)
	v_lshlrev_b32_e32 v54, 16, v172
	v_and_b32_e32 v55, 0xffff0000, v172
	v_lshlrev_b32_e32 v56, 16, v173
	v_and_b32_e32 v57, 0xffff0000, v173
	v_lshlrev_b32_e32 v58, 16, v174
	v_and_b32_e32 v59, 0xffff0000, v174
	v_lshlrev_b32_e32 v60, 16, v175
	v_and_b32_e32 v61, 0xffff0000, v175
	v_pk_mul_f32 v[54:55], v[46:47], v[54:55]
	v_pk_mul_f32 v[56:57], v[46:47], v[56:57]
	v_pk_mul_f32 v[58:59], v[46:47], v[58:59]
	v_pk_mul_f32 v[60:61], v[46:47], v[60:61]
	v_pk_mul_f32 v[54:55], v[224:225], v[54:55]
	v_pk_mul_f32 v[56:57], v[226:227], v[56:57]
	v_pk_mul_f32 v[58:59], v[228:229], v[58:59]
	v_pk_mul_f32 v[60:61], v[230:231], v[60:61]
	v_pk_fma_f32 v[54:55], v[232:233], v[54:55], v[240:241]
	v_pk_fma_f32 v[56:57], v[234:235], v[56:57], v[242:243]
	v_pk_fma_f32 v[58:59], v[236:237], v[58:59], v[244:245]
	v_pk_fma_f32 v[60:61], v[238:239], v[60:61], v[246:247]
	v_med3_f32 v62, v54, s82, v108
	v_med3_f32 v63, v55, s82, v108
	v_med3_f32 v64, v56, s82, v108
	v_med3_f32 v65, v57, s82, v108
	v_med3_f32 v66, v58, s82, v108
	v_med3_f32 v67, v59, s82, v108
	v_med3_f32 v68, v60, s82, v108
	v_med3_f32 v69, v61, s82, v108
	v_cvt_pk_bf16_f32 v192, v54, v55
	v_cvt_pk_bf16_f32 v193, v56, v57
	v_cvt_pk_bf16_f32 v194, v58, v59
	v_cvt_pk_bf16_f32 v195, v60, v61
	v_cvt_pk_fp8_f32 v70, v62, v63
	v_cvt_pk_fp8_f32 v71, v66, v67
	v_cvt_pk_fp8_f32 v70, v64, v65 op_sel:[0,0,1]
	v_cvt_pk_fp8_f32 v71, v68, v69 op_sel:[0,0,1]
	s_nop 0
	global_store_dwordx2 v[72:73], v[70:71], off offset:48
	v_mfma_f32_32x32x16_bf16 v[2:17], v[192:195], v[176:179], v[2:17]
	v_mfma_f32_32x32x16_bf16 v[18:33], v[192:195], v[180:183], v[18:33]
	v_mfma_f32_32x32x16_bf16 v[2:17], v[192:195], v[184:187], v[2:17]
	v_mfma_f32_32x32x16_bf16 v[18:33], v[192:195], v[188:191], v[18:33]
	v_lshlrev_b32_e32 v252, 16, v192
	v_and_b32_e32 v253, 0xffff0000, v192
	v_sub_f32_e32 v62, v54, v252
	v_sub_f32_e32 v63, v55, v253
	v_lshlrev_b32_e32 v252, 16, v193
	v_and_b32_e32 v253, 0xffff0000, v193
	v_sub_f32_e32 v64, v56, v252
	v_sub_f32_e32 v65, v57, v253
	v_lshlrev_b32_e32 v252, 16, v194
	v_and_b32_e32 v253, 0xffff0000, v194
	v_sub_f32_e32 v66, v58, v252
	v_sub_f32_e32 v67, v59, v253
	v_lshlrev_b32_e32 v252, 16, v195
	v_and_b32_e32 v253, 0xffff0000, v195
	v_sub_f32_e32 v68, v60, v252
	v_sub_f32_e32 v69, v61, v253
	v_cvt_pk_bf16_f32 v248, v62, v63
	v_cvt_pk_bf16_f32 v249, v64, v65
	v_cvt_pk_bf16_f32 v250, v66, v67
	v_cvt_pk_bf16_f32 v251, v68, v69
	s_nop 1
	v_mfma_f32_32x32x16_bf16 v[2:17], v[248:251], v[176:179], v[2:17]
	v_mfma_f32_32x32x16_bf16 v[18:33], v[248:251], v[180:183], v[18:33]
	global_load_dwordx4 v[172:175], v[196:197], off offset:224
	global_load_dwordx4 v[176:179], v[34:35], off offset:3072
	global_load_dwordx4 v[180:183], v[36:37], off offset:3072
	global_load_dwordx4 v[184:187], v[38:39], off offset:3072
	global_load_dwordx4 v[188:191], v[40:41], off offset:3072
	s_waitcnt lgkmcnt(0)
	ds_read_b128 v[224:227], v111 offset:320
	ds_read_b128 v[228:231], v111 offset:336
	ds_read_b128 v[232:235], v111 offset:1344
	ds_read_b128 v[236:239], v111 offset:1360
	ds_read_b128 v[240:243], v111 offset:2368
	ds_read_b128 v[244:247], v111 offset:2384
	s_waitcnt vmcnt(18)
	v_lshlrev_b32_e32 v54, 16, v112
	v_and_b32_e32 v55, 0xffff0000, v112
	v_lshlrev_b32_e32 v56, 16, v113
	v_and_b32_e32 v57, 0xffff0000, v113
	v_lshlrev_b32_e32 v58, 16, v114
	v_and_b32_e32 v59, 0xffff0000, v114
	v_lshlrev_b32_e32 v60, 16, v115
	v_and_b32_e32 v61, 0xffff0000, v115
	v_pk_mul_f32 v[54:55], v[46:47], v[54:55]
	v_pk_mul_f32 v[56:57], v[46:47], v[56:57]
	v_pk_mul_f32 v[58:59], v[46:47], v[58:59]
	v_pk_mul_f32 v[60:61], v[46:47], v[60:61]
	v_pk_mul_f32 v[54:55], v[200:201], v[54:55]
	v_pk_mul_f32 v[56:57], v[202:203], v[56:57]
	v_pk_mul_f32 v[58:59], v[204:205], v[58:59]
	v_pk_mul_f32 v[60:61], v[206:207], v[60:61]
	v_pk_fma_f32 v[54:55], v[208:209], v[54:55], v[216:217]
	v_pk_fma_f32 v[56:57], v[210:211], v[56:57], v[218:219]
	v_pk_fma_f32 v[58:59], v[212:213], v[58:59], v[220:221]
	v_pk_fma_f32 v[60:61], v[214:215], v[60:61], v[222:223]
	v_med3_f32 v62, v54, s82, v108
	v_med3_f32 v63, v55, s82, v108
	v_med3_f32 v64, v56, s82, v108
	v_med3_f32 v65, v57, s82, v108
	v_med3_f32 v66, v58, s82, v108
	v_med3_f32 v67, v59, s82, v108
	v_med3_f32 v68, v60, s82, v108
	v_med3_f32 v69, v61, s82, v108
	v_cvt_pk_bf16_f32 v192, v54, v55
	v_cvt_pk_bf16_f32 v193, v56, v57
	v_cvt_pk_bf16_f32 v194, v58, v59
	v_cvt_pk_bf16_f32 v195, v60, v61
	v_cvt_pk_fp8_f32 v70, v62, v63
	v_cvt_pk_fp8_f32 v71, v66, v67
	v_cvt_pk_fp8_f32 v70, v64, v65 op_sel:[0,0,1]
	v_cvt_pk_fp8_f32 v71, v68, v69 op_sel:[0,0,1]
	s_nop 0
	global_store_dwordx2 v[72:73], v[70:71], off offset:64
	v_mfma_f32_32x32x16_bf16 v[2:17], v[192:195], v[116:119], v[2:17]
	v_mfma_f32_32x32x16_bf16 v[18:33], v[192:195], v[120:123], v[18:33]
	v_mfma_f32_32x32x16_bf16 v[2:17], v[192:195], v[124:127], v[2:17]
	v_mfma_f32_32x32x16_bf16 v[18:33], v[192:195], v[128:131], v[18:33]
	v_lshlrev_b32_e32 v252, 16, v192
	v_and_b32_e32 v253, 0xffff0000, v192
	v_sub_f32_e32 v62, v54, v252
	v_sub_f32_e32 v63, v55, v253
	v_lshlrev_b32_e32 v252, 16, v193
	v_and_b32_e32 v253, 0xffff0000, v193
	v_sub_f32_e32 v64, v56, v252
	v_sub_f32_e32 v65, v57, v253
	v_lshlrev_b32_e32 v252, 16, v194
	v_and_b32_e32 v253, 0xffff0000, v194
	v_sub_f32_e32 v66, v58, v252
	v_sub_f32_e32 v67, v59, v253
	v_lshlrev_b32_e32 v252, 16, v195
	v_and_b32_e32 v253, 0xffff0000, v195
	v_sub_f32_e32 v68, v60, v252
	v_sub_f32_e32 v69, v61, v253
	v_cvt_pk_bf16_f32 v248, v62, v63
	v_cvt_pk_bf16_f32 v249, v64, v65
	v_cvt_pk_bf16_f32 v250, v66, v67
	v_cvt_pk_bf16_f32 v251, v68, v69
	s_nop 1
	v_mfma_f32_32x32x16_bf16 v[2:17], v[248:251], v[116:119], v[2:17]
	v_mfma_f32_32x32x16_bf16 v[18:33], v[248:251], v[120:123], v[18:33]
	global_load_dwordx4 v[112:115], v[196:197], off offset:256
	v_lshl_add_u64 v[34:35], v[34:35], 0, v[198:199]
	v_lshl_add_u64 v[36:37], v[36:37], 0, v[198:199]
	v_lshl_add_u64 v[38:39], v[38:39], 0, v[198:199]
	v_lshl_add_u64 v[40:41], v[40:41], 0, v[198:199]
	global_load_dwordx4 v[116:119], v[34:35], off
	global_load_dwordx4 v[120:123], v[36:37], off
	global_load_dwordx4 v[124:127], v[38:39], off
	global_load_dwordx4 v[128:131], v[40:41], off
	s_waitcnt lgkmcnt(0)
	ds_read_b128 v[200:203], v111 offset:384
	ds_read_b128 v[204:207], v111 offset:400
	ds_read_b128 v[208:211], v111 offset:1408
	ds_read_b128 v[212:215], v111 offset:1424
	ds_read_b128 v[216:219], v111 offset:2432
	ds_read_b128 v[220:223], v111 offset:2448
	s_waitcnt vmcnt(18)
	v_lshlrev_b32_e32 v54, 16, v132
	v_and_b32_e32 v55, 0xffff0000, v132
	v_lshlrev_b32_e32 v56, 16, v133
	v_and_b32_e32 v57, 0xffff0000, v133
	v_lshlrev_b32_e32 v58, 16, v134
	v_and_b32_e32 v59, 0xffff0000, v134
	v_lshlrev_b32_e32 v60, 16, v135
	v_and_b32_e32 v61, 0xffff0000, v135
	v_pk_mul_f32 v[54:55], v[46:47], v[54:55]
	v_pk_mul_f32 v[56:57], v[46:47], v[56:57]
	v_pk_mul_f32 v[58:59], v[46:47], v[58:59]
	v_pk_mul_f32 v[60:61], v[46:47], v[60:61]
	v_pk_mul_f32 v[54:55], v[224:225], v[54:55]
	v_pk_mul_f32 v[56:57], v[226:227], v[56:57]
	v_pk_mul_f32 v[58:59], v[228:229], v[58:59]
	v_pk_mul_f32 v[60:61], v[230:231], v[60:61]
	v_pk_fma_f32 v[54:55], v[232:233], v[54:55], v[240:241]
	v_pk_fma_f32 v[56:57], v[234:235], v[56:57], v[242:243]
	v_pk_fma_f32 v[58:59], v[236:237], v[58:59], v[244:245]
	v_pk_fma_f32 v[60:61], v[238:239], v[60:61], v[246:247]
	v_med3_f32 v62, v54, s82, v108
	v_med3_f32 v63, v55, s82, v108
	v_med3_f32 v64, v56, s82, v108
	v_med3_f32 v65, v57, s82, v108
	v_med3_f32 v66, v58, s82, v108
	v_med3_f32 v67, v59, s82, v108
	v_med3_f32 v68, v60, s82, v108
	v_med3_f32 v69, v61, s82, v108
	v_cvt_pk_bf16_f32 v192, v54, v55
	v_cvt_pk_bf16_f32 v193, v56, v57
	v_cvt_pk_bf16_f32 v194, v58, v59
	v_cvt_pk_bf16_f32 v195, v60, v61
	v_cvt_pk_fp8_f32 v70, v62, v63
	v_cvt_pk_fp8_f32 v71, v66, v67
	v_cvt_pk_fp8_f32 v70, v64, v65 op_sel:[0,0,1]
	v_cvt_pk_fp8_f32 v71, v68, v69 op_sel:[0,0,1]
	s_nop 0
	global_store_dwordx2 v[72:73], v[70:71], off offset:80
	v_mfma_f32_32x32x16_bf16 v[2:17], v[192:195], v[136:139], v[2:17]
	v_mfma_f32_32x32x16_bf16 v[18:33], v[192:195], v[140:143], v[18:33]
	v_mfma_f32_32x32x16_bf16 v[2:17], v[192:195], v[144:147], v[2:17]
	v_mfma_f32_32x32x16_bf16 v[18:33], v[192:195], v[148:151], v[18:33]
	v_lshlrev_b32_e32 v252, 16, v192
	v_and_b32_e32 v253, 0xffff0000, v192
	v_sub_f32_e32 v62, v54, v252
	v_sub_f32_e32 v63, v55, v253
	v_lshlrev_b32_e32 v252, 16, v193
	v_and_b32_e32 v253, 0xffff0000, v193
	v_sub_f32_e32 v64, v56, v252
	v_sub_f32_e32 v65, v57, v253
	v_lshlrev_b32_e32 v252, 16, v194
	v_and_b32_e32 v253, 0xffff0000, v194
	v_sub_f32_e32 v66, v58, v252
	v_sub_f32_e32 v67, v59, v253
	v_lshlrev_b32_e32 v252, 16, v195
	v_and_b32_e32 v253, 0xffff0000, v195
	v_sub_f32_e32 v68, v60, v252
	v_sub_f32_e32 v69, v61, v253
	v_cvt_pk_bf16_f32 v248, v62, v63
	v_cvt_pk_bf16_f32 v249, v64, v65
	v_cvt_pk_bf16_f32 v250, v66, v67
	v_cvt_pk_bf16_f32 v251, v68, v69
	s_nop 1
	v_mfma_f32_32x32x16_bf16 v[2:17], v[248:251], v[136:139], v[2:17]
	v_mfma_f32_32x32x16_bf16 v[18:33], v[248:251], v[140:143], v[18:33]
	global_load_dwordx4 v[132:135], v[196:197], off offset:288
	global_load_dwordx4 v[136:139], v[34:35], off offset:1024
	global_load_dwordx4 v[140:143], v[36:37], off offset:1024
	global_load_dwordx4 v[144:147], v[38:39], off offset:1024
	global_load_dwordx4 v[148:151], v[40:41], off offset:1024
	s_waitcnt lgkmcnt(0)
	ds_read_b128 v[224:227], v111 offset:448
	ds_read_b128 v[228:231], v111 offset:464
	ds_read_b128 v[232:235], v111 offset:1472
	ds_read_b128 v[236:239], v111 offset:1488
	ds_read_b128 v[240:243], v111 offset:2496
	ds_read_b128 v[244:247], v111 offset:2512
	s_waitcnt vmcnt(18)
	v_lshlrev_b32_e32 v54, 16, v152
	v_and_b32_e32 v55, 0xffff0000, v152
	v_lshlrev_b32_e32 v56, 16, v153
	v_and_b32_e32 v57, 0xffff0000, v153
	v_lshlrev_b32_e32 v58, 16, v154
	v_and_b32_e32 v59, 0xffff0000, v154
	v_lshlrev_b32_e32 v60, 16, v155
	v_and_b32_e32 v61, 0xffff0000, v155
	v_pk_mul_f32 v[54:55], v[46:47], v[54:55]
	v_pk_mul_f32 v[56:57], v[46:47], v[56:57]
	v_pk_mul_f32 v[58:59], v[46:47], v[58:59]
	v_pk_mul_f32 v[60:61], v[46:47], v[60:61]
	v_pk_mul_f32 v[54:55], v[200:201], v[54:55]
	v_pk_mul_f32 v[56:57], v[202:203], v[56:57]
	v_pk_mul_f32 v[58:59], v[204:205], v[58:59]
	v_pk_mul_f32 v[60:61], v[206:207], v[60:61]
	v_pk_fma_f32 v[54:55], v[208:209], v[54:55], v[216:217]
	v_pk_fma_f32 v[56:57], v[210:211], v[56:57], v[218:219]
	v_pk_fma_f32 v[58:59], v[212:213], v[58:59], v[220:221]
	v_pk_fma_f32 v[60:61], v[214:215], v[60:61], v[222:223]
	v_med3_f32 v62, v54, s82, v108
	v_med3_f32 v63, v55, s82, v108
	v_med3_f32 v64, v56, s82, v108
	v_med3_f32 v65, v57, s82, v108
	v_med3_f32 v66, v58, s82, v108
	v_med3_f32 v67, v59, s82, v108
	v_med3_f32 v68, v60, s82, v108
	v_med3_f32 v69, v61, s82, v108
	v_cvt_pk_bf16_f32 v192, v54, v55
	v_cvt_pk_bf16_f32 v193, v56, v57
	v_cvt_pk_bf16_f32 v194, v58, v59
	v_cvt_pk_bf16_f32 v195, v60, v61
	v_cvt_pk_fp8_f32 v70, v62, v63
	v_cvt_pk_fp8_f32 v71, v66, v67
	v_cvt_pk_fp8_f32 v70, v64, v65 op_sel:[0,0,1]
	v_cvt_pk_fp8_f32 v71, v68, v69 op_sel:[0,0,1]
	s_nop 0
	global_store_dwordx2 v[72:73], v[70:71], off offset:96
	v_mfma_f32_32x32x16_bf16 v[2:17], v[192:195], v[156:159], v[2:17]
	v_mfma_f32_32x32x16_bf16 v[18:33], v[192:195], v[160:163], v[18:33]
	v_mfma_f32_32x32x16_bf16 v[2:17], v[192:195], v[164:167], v[2:17]
	v_mfma_f32_32x32x16_bf16 v[18:33], v[192:195], v[168:171], v[18:33]
	v_lshlrev_b32_e32 v252, 16, v192
	v_and_b32_e32 v253, 0xffff0000, v192
	v_sub_f32_e32 v62, v54, v252
	v_sub_f32_e32 v63, v55, v253
	v_lshlrev_b32_e32 v252, 16, v193
	v_and_b32_e32 v253, 0xffff0000, v193
	v_sub_f32_e32 v64, v56, v252
	v_sub_f32_e32 v65, v57, v253
	v_lshlrev_b32_e32 v252, 16, v194
	v_and_b32_e32 v253, 0xffff0000, v194
	v_sub_f32_e32 v66, v58, v252
	v_sub_f32_e32 v67, v59, v253
	v_lshlrev_b32_e32 v252, 16, v195
	v_and_b32_e32 v253, 0xffff0000, v195
	v_sub_f32_e32 v68, v60, v252
	v_sub_f32_e32 v69, v61, v253
	v_cvt_pk_bf16_f32 v248, v62, v63
	v_cvt_pk_bf16_f32 v249, v64, v65
	v_cvt_pk_bf16_f32 v250, v66, v67
	v_cvt_pk_bf16_f32 v251, v68, v69
	s_nop 1
	v_mfma_f32_32x32x16_bf16 v[2:17], v[248:251], v[156:159], v[2:17]
	v_mfma_f32_32x32x16_bf16 v[18:33], v[248:251], v[160:163], v[18:33]
	global_load_dwordx4 v[152:155], v[196:197], off offset:320
	global_load_dwordx4 v[156:159], v[34:35], off offset:2048
	global_load_dwordx4 v[160:163], v[36:37], off offset:2048
	global_load_dwordx4 v[164:167], v[38:39], off offset:2048
	global_load_dwordx4 v[168:171], v[40:41], off offset:2048
	s_waitcnt lgkmcnt(0)
	ds_read_b128 v[200:203], v111 offset:512
	ds_read_b128 v[204:207], v111 offset:528
	ds_read_b128 v[208:211], v111 offset:1536
	ds_read_b128 v[212:215], v111 offset:1552
	ds_read_b128 v[216:219], v111 offset:2560
	ds_read_b128 v[220:223], v111 offset:2576
	s_waitcnt vmcnt(18)
	v_lshlrev_b32_e32 v54, 16, v172
	v_and_b32_e32 v55, 0xffff0000, v172
	v_lshlrev_b32_e32 v56, 16, v173
	v_and_b32_e32 v57, 0xffff0000, v173
	v_lshlrev_b32_e32 v58, 16, v174
	v_and_b32_e32 v59, 0xffff0000, v174
	v_lshlrev_b32_e32 v60, 16, v175
	v_and_b32_e32 v61, 0xffff0000, v175
	v_pk_mul_f32 v[54:55], v[46:47], v[54:55]
	v_pk_mul_f32 v[56:57], v[46:47], v[56:57]
	v_pk_mul_f32 v[58:59], v[46:47], v[58:59]
	v_pk_mul_f32 v[60:61], v[46:47], v[60:61]
	v_pk_mul_f32 v[54:55], v[224:225], v[54:55]
	v_pk_mul_f32 v[56:57], v[226:227], v[56:57]
	v_pk_mul_f32 v[58:59], v[228:229], v[58:59]
	v_pk_mul_f32 v[60:61], v[230:231], v[60:61]
	v_pk_fma_f32 v[54:55], v[232:233], v[54:55], v[240:241]
	v_pk_fma_f32 v[56:57], v[234:235], v[56:57], v[242:243]
	v_pk_fma_f32 v[58:59], v[236:237], v[58:59], v[244:245]
	v_pk_fma_f32 v[60:61], v[238:239], v[60:61], v[246:247]
	v_med3_f32 v62, v54, s82, v108
	v_med3_f32 v63, v55, s82, v108
	v_med3_f32 v64, v56, s82, v108
	v_med3_f32 v65, v57, s82, v108
	v_med3_f32 v66, v58, s82, v108
	v_med3_f32 v67, v59, s82, v108
	v_med3_f32 v68, v60, s82, v108
	v_med3_f32 v69, v61, s82, v108
	v_cvt_pk_bf16_f32 v192, v54, v55
	v_cvt_pk_bf16_f32 v193, v56, v57
	v_cvt_pk_bf16_f32 v194, v58, v59
	v_cvt_pk_bf16_f32 v195, v60, v61
	v_cvt_pk_fp8_f32 v70, v62, v63
	v_cvt_pk_fp8_f32 v71, v66, v67
	v_cvt_pk_fp8_f32 v70, v64, v65 op_sel:[0,0,1]
	v_cvt_pk_fp8_f32 v71, v68, v69 op_sel:[0,0,1]
	s_nop 0
	global_store_dwordx2 v[72:73], v[70:71], off offset:112
	v_mfma_f32_32x32x16_bf16 v[2:17], v[192:195], v[176:179], v[2:17]
	v_mfma_f32_32x32x16_bf16 v[18:33], v[192:195], v[180:183], v[18:33]
	v_mfma_f32_32x32x16_bf16 v[2:17], v[192:195], v[184:187], v[2:17]
	v_mfma_f32_32x32x16_bf16 v[18:33], v[192:195], v[188:191], v[18:33]
	v_lshlrev_b32_e32 v252, 16, v192
	v_and_b32_e32 v253, 0xffff0000, v192
	v_sub_f32_e32 v62, v54, v252
	v_sub_f32_e32 v63, v55, v253
	v_lshlrev_b32_e32 v252, 16, v193
	v_and_b32_e32 v253, 0xffff0000, v193
	v_sub_f32_e32 v64, v56, v252
	v_sub_f32_e32 v65, v57, v253
	v_lshlrev_b32_e32 v252, 16, v194
	v_and_b32_e32 v253, 0xffff0000, v194
	v_sub_f32_e32 v66, v58, v252
	v_sub_f32_e32 v67, v59, v253
	v_lshlrev_b32_e32 v252, 16, v195
	v_and_b32_e32 v253, 0xffff0000, v195
	v_sub_f32_e32 v68, v60, v252
	v_sub_f32_e32 v69, v61, v253
	v_cvt_pk_bf16_f32 v248, v62, v63
	v_cvt_pk_bf16_f32 v249, v64, v65
	v_cvt_pk_bf16_f32 v250, v66, v67
	v_cvt_pk_bf16_f32 v251, v68, v69
	s_nop 1
	v_mfma_f32_32x32x16_bf16 v[2:17], v[248:251], v[176:179], v[2:17]
	v_mfma_f32_32x32x16_bf16 v[18:33], v[248:251], v[180:183], v[18:33]
	global_load_dwordx4 v[172:175], v[196:197], off offset:352
	global_load_dwordx4 v[176:179], v[34:35], off offset:3072
	global_load_dwordx4 v[180:183], v[36:37], off offset:3072
	global_load_dwordx4 v[184:187], v[38:39], off offset:3072
	global_load_dwordx4 v[188:191], v[40:41], off offset:3072
	s_waitcnt lgkmcnt(0)
	ds_read_b128 v[224:227], v111 offset:576
	ds_read_b128 v[228:231], v111 offset:592
	ds_read_b128 v[232:235], v111 offset:1600
	ds_read_b128 v[236:239], v111 offset:1616
	ds_read_b128 v[240:243], v111 offset:2624
	ds_read_b128 v[244:247], v111 offset:2640
	s_waitcnt vmcnt(18)
	v_lshlrev_b32_e32 v54, 16, v112
	v_and_b32_e32 v55, 0xffff0000, v112
	v_lshlrev_b32_e32 v56, 16, v113
	v_and_b32_e32 v57, 0xffff0000, v113
	v_lshlrev_b32_e32 v58, 16, v114
	v_and_b32_e32 v59, 0xffff0000, v114
	v_lshlrev_b32_e32 v60, 16, v115
	v_and_b32_e32 v61, 0xffff0000, v115
	v_pk_mul_f32 v[54:55], v[46:47], v[54:55]
	v_pk_mul_f32 v[56:57], v[46:47], v[56:57]
	v_pk_mul_f32 v[58:59], v[46:47], v[58:59]
	v_pk_mul_f32 v[60:61], v[46:47], v[60:61]
	v_pk_mul_f32 v[54:55], v[200:201], v[54:55]
	v_pk_mul_f32 v[56:57], v[202:203], v[56:57]
	v_pk_mul_f32 v[58:59], v[204:205], v[58:59]
	v_pk_mul_f32 v[60:61], v[206:207], v[60:61]
	v_pk_fma_f32 v[54:55], v[208:209], v[54:55], v[216:217]
	v_pk_fma_f32 v[56:57], v[210:211], v[56:57], v[218:219]
	v_pk_fma_f32 v[58:59], v[212:213], v[58:59], v[220:221]
	v_pk_fma_f32 v[60:61], v[214:215], v[60:61], v[222:223]
	v_med3_f32 v62, v54, s82, v108
	v_med3_f32 v63, v55, s82, v108
	v_med3_f32 v64, v56, s82, v108
	v_med3_f32 v65, v57, s82, v108
	v_med3_f32 v66, v58, s82, v108
	v_med3_f32 v67, v59, s82, v108
	v_med3_f32 v68, v60, s82, v108
	v_med3_f32 v69, v61, s82, v108
	v_cvt_pk_bf16_f32 v192, v54, v55
	v_cvt_pk_bf16_f32 v193, v56, v57
	v_cvt_pk_bf16_f32 v194, v58, v59
	v_cvt_pk_bf16_f32 v195, v60, v61
	v_cvt_pk_fp8_f32 v70, v62, v63
	v_cvt_pk_fp8_f32 v71, v66, v67
	v_cvt_pk_fp8_f32 v70, v64, v65 op_sel:[0,0,1]
	v_cvt_pk_fp8_f32 v71, v68, v69 op_sel:[0,0,1]
	s_nop 0
	global_store_dwordx2 v[72:73], v[70:71], off offset:128
	v_mfma_f32_32x32x16_bf16 v[2:17], v[192:195], v[116:119], v[2:17]
	v_mfma_f32_32x32x16_bf16 v[18:33], v[192:195], v[120:123], v[18:33]
	v_mfma_f32_32x32x16_bf16 v[2:17], v[192:195], v[124:127], v[2:17]
	v_mfma_f32_32x32x16_bf16 v[18:33], v[192:195], v[128:131], v[18:33]
	v_lshlrev_b32_e32 v252, 16, v192
	v_and_b32_e32 v253, 0xffff0000, v192
	v_sub_f32_e32 v62, v54, v252
	v_sub_f32_e32 v63, v55, v253
	v_lshlrev_b32_e32 v252, 16, v193
	v_and_b32_e32 v253, 0xffff0000, v193
	v_sub_f32_e32 v64, v56, v252
	v_sub_f32_e32 v65, v57, v253
	v_lshlrev_b32_e32 v252, 16, v194
	v_and_b32_e32 v253, 0xffff0000, v194
	v_sub_f32_e32 v66, v58, v252
	v_sub_f32_e32 v67, v59, v253
	v_lshlrev_b32_e32 v252, 16, v195
	v_and_b32_e32 v253, 0xffff0000, v195
	v_sub_f32_e32 v68, v60, v252
	v_sub_f32_e32 v69, v61, v253
	v_cvt_pk_bf16_f32 v248, v62, v63
	v_cvt_pk_bf16_f32 v249, v64, v65
	v_cvt_pk_bf16_f32 v250, v66, v67
	v_cvt_pk_bf16_f32 v251, v68, v69
	s_nop 1
	v_mfma_f32_32x32x16_bf16 v[2:17], v[248:251], v[116:119], v[2:17]
	v_mfma_f32_32x32x16_bf16 v[18:33], v[248:251], v[120:123], v[18:33]
	global_load_dwordx4 v[112:115], v[196:197], off offset:384
	v_lshl_add_u64 v[34:35], v[34:35], 0, v[198:199]
	v_lshl_add_u64 v[36:37], v[36:37], 0, v[198:199]
	v_lshl_add_u64 v[38:39], v[38:39], 0, v[198:199]
	v_lshl_add_u64 v[40:41], v[40:41], 0, v[198:199]
	global_load_dwordx4 v[116:119], v[34:35], off
	global_load_dwordx4 v[120:123], v[36:37], off
	global_load_dwordx4 v[124:127], v[38:39], off
	global_load_dwordx4 v[128:131], v[40:41], off
	s_waitcnt lgkmcnt(0)
	ds_read_b128 v[200:203], v111 offset:640
	ds_read_b128 v[204:207], v111 offset:656
	ds_read_b128 v[208:211], v111 offset:1664
	ds_read_b128 v[212:215], v111 offset:1680
	ds_read_b128 v[216:219], v111 offset:2688
	ds_read_b128 v[220:223], v111 offset:2704
	s_waitcnt vmcnt(18)
	v_lshlrev_b32_e32 v54, 16, v132
	v_and_b32_e32 v55, 0xffff0000, v132
	v_lshlrev_b32_e32 v56, 16, v133
	v_and_b32_e32 v57, 0xffff0000, v133
	v_lshlrev_b32_e32 v58, 16, v134
	v_and_b32_e32 v59, 0xffff0000, v134
	v_lshlrev_b32_e32 v60, 16, v135
	v_and_b32_e32 v61, 0xffff0000, v135
	v_pk_mul_f32 v[54:55], v[46:47], v[54:55]
	v_pk_mul_f32 v[56:57], v[46:47], v[56:57]
	v_pk_mul_f32 v[58:59], v[46:47], v[58:59]
	v_pk_mul_f32 v[60:61], v[46:47], v[60:61]
	v_pk_mul_f32 v[54:55], v[224:225], v[54:55]
	v_pk_mul_f32 v[56:57], v[226:227], v[56:57]
	v_pk_mul_f32 v[58:59], v[228:229], v[58:59]
	v_pk_mul_f32 v[60:61], v[230:231], v[60:61]
	v_pk_fma_f32 v[54:55], v[232:233], v[54:55], v[240:241]
	v_pk_fma_f32 v[56:57], v[234:235], v[56:57], v[242:243]
	v_pk_fma_f32 v[58:59], v[236:237], v[58:59], v[244:245]
	v_pk_fma_f32 v[60:61], v[238:239], v[60:61], v[246:247]
	v_med3_f32 v62, v54, s82, v108
	v_med3_f32 v63, v55, s82, v108
	v_med3_f32 v64, v56, s82, v108
	v_med3_f32 v65, v57, s82, v108
	v_med3_f32 v66, v58, s82, v108
	v_med3_f32 v67, v59, s82, v108
	v_med3_f32 v68, v60, s82, v108
	v_med3_f32 v69, v61, s82, v108
	v_cvt_pk_bf16_f32 v192, v54, v55
	v_cvt_pk_bf16_f32 v193, v56, v57
	v_cvt_pk_bf16_f32 v194, v58, v59
	v_cvt_pk_bf16_f32 v195, v60, v61
	v_cvt_pk_fp8_f32 v70, v62, v63
	v_cvt_pk_fp8_f32 v71, v66, v67
	v_cvt_pk_fp8_f32 v70, v64, v65 op_sel:[0,0,1]
	v_cvt_pk_fp8_f32 v71, v68, v69 op_sel:[0,0,1]
	s_nop 0
	global_store_dwordx2 v[72:73], v[70:71], off offset:144
	v_mfma_f32_32x32x16_bf16 v[2:17], v[192:195], v[136:139], v[2:17]
	v_mfma_f32_32x32x16_bf16 v[18:33], v[192:195], v[140:143], v[18:33]
	v_mfma_f32_32x32x16_bf16 v[2:17], v[192:195], v[144:147], v[2:17]
	v_mfma_f32_32x32x16_bf16 v[18:33], v[192:195], v[148:151], v[18:33]
	v_lshlrev_b32_e32 v252, 16, v192
	v_and_b32_e32 v253, 0xffff0000, v192
	v_sub_f32_e32 v62, v54, v252
	v_sub_f32_e32 v63, v55, v253
	v_lshlrev_b32_e32 v252, 16, v193
	v_and_b32_e32 v253, 0xffff0000, v193
	v_sub_f32_e32 v64, v56, v252
	v_sub_f32_e32 v65, v57, v253
	v_lshlrev_b32_e32 v252, 16, v194
	v_and_b32_e32 v253, 0xffff0000, v194
	v_sub_f32_e32 v66, v58, v252
	v_sub_f32_e32 v67, v59, v253
	v_lshlrev_b32_e32 v252, 16, v195
	v_and_b32_e32 v253, 0xffff0000, v195
	v_sub_f32_e32 v68, v60, v252
	v_sub_f32_e32 v69, v61, v253
	v_cvt_pk_bf16_f32 v248, v62, v63
	v_cvt_pk_bf16_f32 v249, v64, v65
	v_cvt_pk_bf16_f32 v250, v66, v67
	v_cvt_pk_bf16_f32 v251, v68, v69
	s_nop 1
	v_mfma_f32_32x32x16_bf16 v[2:17], v[248:251], v[136:139], v[2:17]
	v_mfma_f32_32x32x16_bf16 v[18:33], v[248:251], v[140:143], v[18:33]
	global_load_dwordx4 v[132:135], v[196:197], off offset:416
	global_load_dwordx4 v[136:139], v[34:35], off offset:1024
	global_load_dwordx4 v[140:143], v[36:37], off offset:1024
	global_load_dwordx4 v[144:147], v[38:39], off offset:1024
	global_load_dwordx4 v[148:151], v[40:41], off offset:1024
	s_waitcnt lgkmcnt(0)
	ds_read_b128 v[224:227], v111 offset:704
	ds_read_b128 v[228:231], v111 offset:720
	ds_read_b128 v[232:235], v111 offset:1728
	ds_read_b128 v[236:239], v111 offset:1744
	ds_read_b128 v[240:243], v111 offset:2752
	ds_read_b128 v[244:247], v111 offset:2768
	s_waitcnt vmcnt(18)
	v_lshlrev_b32_e32 v54, 16, v152
	v_and_b32_e32 v55, 0xffff0000, v152
	v_lshlrev_b32_e32 v56, 16, v153
	v_and_b32_e32 v57, 0xffff0000, v153
	v_lshlrev_b32_e32 v58, 16, v154
	v_and_b32_e32 v59, 0xffff0000, v154
	v_lshlrev_b32_e32 v60, 16, v155
	v_and_b32_e32 v61, 0xffff0000, v155
	v_pk_mul_f32 v[54:55], v[46:47], v[54:55]
	v_pk_mul_f32 v[56:57], v[46:47], v[56:57]
	v_pk_mul_f32 v[58:59], v[46:47], v[58:59]
	v_pk_mul_f32 v[60:61], v[46:47], v[60:61]
	v_pk_mul_f32 v[54:55], v[200:201], v[54:55]
	v_pk_mul_f32 v[56:57], v[202:203], v[56:57]
	v_pk_mul_f32 v[58:59], v[204:205], v[58:59]
	v_pk_mul_f32 v[60:61], v[206:207], v[60:61]
	v_pk_fma_f32 v[54:55], v[208:209], v[54:55], v[216:217]
	v_pk_fma_f32 v[56:57], v[210:211], v[56:57], v[218:219]
	v_pk_fma_f32 v[58:59], v[212:213], v[58:59], v[220:221]
	v_pk_fma_f32 v[60:61], v[214:215], v[60:61], v[222:223]
	v_med3_f32 v62, v54, s82, v108
	v_med3_f32 v63, v55, s82, v108
	v_med3_f32 v64, v56, s82, v108
	v_med3_f32 v65, v57, s82, v108
	v_med3_f32 v66, v58, s82, v108
	v_med3_f32 v67, v59, s82, v108
	v_med3_f32 v68, v60, s82, v108
	v_med3_f32 v69, v61, s82, v108
	v_cvt_pk_bf16_f32 v192, v54, v55
	v_cvt_pk_bf16_f32 v193, v56, v57
	v_cvt_pk_bf16_f32 v194, v58, v59
	v_cvt_pk_bf16_f32 v195, v60, v61
	v_cvt_pk_fp8_f32 v70, v62, v63
	v_cvt_pk_fp8_f32 v71, v66, v67
	v_cvt_pk_fp8_f32 v70, v64, v65 op_sel:[0,0,1]
	v_cvt_pk_fp8_f32 v71, v68, v69 op_sel:[0,0,1]
	s_nop 0
	global_store_dwordx2 v[72:73], v[70:71], off offset:160
	v_mfma_f32_32x32x16_bf16 v[2:17], v[192:195], v[156:159], v[2:17]
	v_mfma_f32_32x32x16_bf16 v[18:33], v[192:195], v[160:163], v[18:33]
	v_mfma_f32_32x32x16_bf16 v[2:17], v[192:195], v[164:167], v[2:17]
	v_mfma_f32_32x32x16_bf16 v[18:33], v[192:195], v[168:171], v[18:33]
	v_lshlrev_b32_e32 v252, 16, v192
	v_and_b32_e32 v253, 0xffff0000, v192
	v_sub_f32_e32 v62, v54, v252
	v_sub_f32_e32 v63, v55, v253
	v_lshlrev_b32_e32 v252, 16, v193
	v_and_b32_e32 v253, 0xffff0000, v193
	v_sub_f32_e32 v64, v56, v252
	v_sub_f32_e32 v65, v57, v253
	v_lshlrev_b32_e32 v252, 16, v194
	v_and_b32_e32 v253, 0xffff0000, v194
	v_sub_f32_e32 v66, v58, v252
	v_sub_f32_e32 v67, v59, v253
	v_lshlrev_b32_e32 v252, 16, v195
	v_and_b32_e32 v253, 0xffff0000, v195
	v_sub_f32_e32 v68, v60, v252
	v_sub_f32_e32 v69, v61, v253
	v_cvt_pk_bf16_f32 v248, v62, v63
	v_cvt_pk_bf16_f32 v249, v64, v65
	v_cvt_pk_bf16_f32 v250, v66, v67
	v_cvt_pk_bf16_f32 v251, v68, v69
	s_nop 1
	v_mfma_f32_32x32x16_bf16 v[2:17], v[248:251], v[156:159], v[2:17]
	v_mfma_f32_32x32x16_bf16 v[18:33], v[248:251], v[160:163], v[18:33]
	global_load_dwordx4 v[152:155], v[196:197], off offset:448
	global_load_dwordx4 v[156:159], v[34:35], off offset:2048
	global_load_dwordx4 v[160:163], v[36:37], off offset:2048
	global_load_dwordx4 v[164:167], v[38:39], off offset:2048
	global_load_dwordx4 v[168:171], v[40:41], off offset:2048
	s_waitcnt lgkmcnt(0)
	ds_read_b128 v[200:203], v111 offset:768
	ds_read_b128 v[204:207], v111 offset:784
	ds_read_b128 v[208:211], v111 offset:1792
	ds_read_b128 v[212:215], v111 offset:1808
	ds_read_b128 v[216:219], v111 offset:2816
	ds_read_b128 v[220:223], v111 offset:2832
	s_waitcnt vmcnt(18)
	v_lshlrev_b32_e32 v54, 16, v172
	v_and_b32_e32 v55, 0xffff0000, v172
	v_lshlrev_b32_e32 v56, 16, v173
	v_and_b32_e32 v57, 0xffff0000, v173
	v_lshlrev_b32_e32 v58, 16, v174
	v_and_b32_e32 v59, 0xffff0000, v174
	v_lshlrev_b32_e32 v60, 16, v175
	v_and_b32_e32 v61, 0xffff0000, v175
	v_pk_mul_f32 v[54:55], v[46:47], v[54:55]
	v_pk_mul_f32 v[56:57], v[46:47], v[56:57]
	v_pk_mul_f32 v[58:59], v[46:47], v[58:59]
	v_pk_mul_f32 v[60:61], v[46:47], v[60:61]
	v_pk_mul_f32 v[54:55], v[224:225], v[54:55]
	v_pk_mul_f32 v[56:57], v[226:227], v[56:57]
	v_pk_mul_f32 v[58:59], v[228:229], v[58:59]
	v_pk_mul_f32 v[60:61], v[230:231], v[60:61]
	v_pk_fma_f32 v[54:55], v[232:233], v[54:55], v[240:241]
	v_pk_fma_f32 v[56:57], v[234:235], v[56:57], v[242:243]
	v_pk_fma_f32 v[58:59], v[236:237], v[58:59], v[244:245]
	v_pk_fma_f32 v[60:61], v[238:239], v[60:61], v[246:247]
	v_med3_f32 v62, v54, s82, v108
	v_med3_f32 v63, v55, s82, v108
	v_med3_f32 v64, v56, s82, v108
	v_med3_f32 v65, v57, s82, v108
	v_med3_f32 v66, v58, s82, v108
	v_med3_f32 v67, v59, s82, v108
	v_med3_f32 v68, v60, s82, v108
	v_med3_f32 v69, v61, s82, v108
	v_cvt_pk_bf16_f32 v192, v54, v55
	v_cvt_pk_bf16_f32 v193, v56, v57
	v_cvt_pk_bf16_f32 v194, v58, v59
	v_cvt_pk_bf16_f32 v195, v60, v61
	v_cvt_pk_fp8_f32 v70, v62, v63
	v_cvt_pk_fp8_f32 v71, v66, v67
	v_cvt_pk_fp8_f32 v70, v64, v65 op_sel:[0,0,1]
	v_cvt_pk_fp8_f32 v71, v68, v69 op_sel:[0,0,1]
	s_nop 0
	global_store_dwordx2 v[72:73], v[70:71], off offset:176
	v_mfma_f32_32x32x16_bf16 v[2:17], v[192:195], v[176:179], v[2:17]
	v_mfma_f32_32x32x16_bf16 v[18:33], v[192:195], v[180:183], v[18:33]
	v_mfma_f32_32x32x16_bf16 v[2:17], v[192:195], v[184:187], v[2:17]
	v_mfma_f32_32x32x16_bf16 v[18:33], v[192:195], v[188:191], v[18:33]
	v_lshlrev_b32_e32 v252, 16, v192
	v_and_b32_e32 v253, 0xffff0000, v192
	v_sub_f32_e32 v62, v54, v252
	v_sub_f32_e32 v63, v55, v253
	v_lshlrev_b32_e32 v252, 16, v193
	v_and_b32_e32 v253, 0xffff0000, v193
	v_sub_f32_e32 v64, v56, v252
	v_sub_f32_e32 v65, v57, v253
	v_lshlrev_b32_e32 v252, 16, v194
	v_and_b32_e32 v253, 0xffff0000, v194
	v_sub_f32_e32 v66, v58, v252
	v_sub_f32_e32 v67, v59, v253
	v_lshlrev_b32_e32 v252, 16, v195
	v_and_b32_e32 v253, 0xffff0000, v195
	v_sub_f32_e32 v68, v60, v252
	v_sub_f32_e32 v69, v61, v253
	v_cvt_pk_bf16_f32 v248, v62, v63
	v_cvt_pk_bf16_f32 v249, v64, v65
	v_cvt_pk_bf16_f32 v250, v66, v67
	v_cvt_pk_bf16_f32 v251, v68, v69
	s_nop 1
	v_mfma_f32_32x32x16_bf16 v[2:17], v[248:251], v[176:179], v[2:17]
	v_mfma_f32_32x32x16_bf16 v[18:33], v[248:251], v[180:183], v[18:33]
	global_load_dwordx4 v[172:175], v[196:197], off offset:480
	global_load_dwordx4 v[176:179], v[34:35], off offset:3072
	global_load_dwordx4 v[180:183], v[36:37], off offset:3072
	global_load_dwordx4 v[184:187], v[38:39], off offset:3072
	global_load_dwordx4 v[188:191], v[40:41], off offset:3072
	s_waitcnt lgkmcnt(0)
	ds_read_b128 v[224:227], v111 offset:832
	ds_read_b128 v[228:231], v111 offset:848
	ds_read_b128 v[232:235], v111 offset:1856
	ds_read_b128 v[236:239], v111 offset:1872
	ds_read_b128 v[240:243], v111 offset:2880
	ds_read_b128 v[244:247], v111 offset:2896
	s_waitcnt vmcnt(18)
	v_lshlrev_b32_e32 v54, 16, v112
	v_and_b32_e32 v55, 0xffff0000, v112
	v_lshlrev_b32_e32 v56, 16, v113
	v_and_b32_e32 v57, 0xffff0000, v113
	v_lshlrev_b32_e32 v58, 16, v114
	v_and_b32_e32 v59, 0xffff0000, v114
	v_lshlrev_b32_e32 v60, 16, v115
	v_and_b32_e32 v61, 0xffff0000, v115
	v_pk_mul_f32 v[54:55], v[46:47], v[54:55]
	v_pk_mul_f32 v[56:57], v[46:47], v[56:57]
	v_pk_mul_f32 v[58:59], v[46:47], v[58:59]
	v_pk_mul_f32 v[60:61], v[46:47], v[60:61]
	v_pk_mul_f32 v[54:55], v[200:201], v[54:55]
	v_pk_mul_f32 v[56:57], v[202:203], v[56:57]
	v_pk_mul_f32 v[58:59], v[204:205], v[58:59]
	v_pk_mul_f32 v[60:61], v[206:207], v[60:61]
	v_pk_fma_f32 v[54:55], v[208:209], v[54:55], v[216:217]
	v_pk_fma_f32 v[56:57], v[210:211], v[56:57], v[218:219]
	v_pk_fma_f32 v[58:59], v[212:213], v[58:59], v[220:221]
	v_pk_fma_f32 v[60:61], v[214:215], v[60:61], v[222:223]
	v_med3_f32 v62, v54, s82, v108
	v_med3_f32 v63, v55, s82, v108
	v_med3_f32 v64, v56, s82, v108
	v_med3_f32 v65, v57, s82, v108
	v_med3_f32 v66, v58, s82, v108
	v_med3_f32 v67, v59, s82, v108
	v_med3_f32 v68, v60, s82, v108
	v_med3_f32 v69, v61, s82, v108
	v_cvt_pk_bf16_f32 v192, v54, v55
	v_cvt_pk_bf16_f32 v193, v56, v57
	v_cvt_pk_bf16_f32 v194, v58, v59
	v_cvt_pk_bf16_f32 v195, v60, v61
	v_cvt_pk_fp8_f32 v70, v62, v63
	v_cvt_pk_fp8_f32 v71, v66, v67
	v_cvt_pk_fp8_f32 v70, v64, v65 op_sel:[0,0,1]
	v_cvt_pk_fp8_f32 v71, v68, v69 op_sel:[0,0,1]
	s_nop 0
	global_store_dwordx2 v[72:73], v[70:71], off offset:192
	v_mfma_f32_32x32x16_bf16 v[2:17], v[192:195], v[116:119], v[2:17]
	v_mfma_f32_32x32x16_bf16 v[18:33], v[192:195], v[120:123], v[18:33]
	v_mfma_f32_32x32x16_bf16 v[2:17], v[192:195], v[124:127], v[2:17]
	v_mfma_f32_32x32x16_bf16 v[18:33], v[192:195], v[128:131], v[18:33]
	v_lshlrev_b32_e32 v252, 16, v192
	v_and_b32_e32 v253, 0xffff0000, v192
	v_sub_f32_e32 v62, v54, v252
	v_sub_f32_e32 v63, v55, v253
	v_lshlrev_b32_e32 v252, 16, v193
	v_and_b32_e32 v253, 0xffff0000, v193
	v_sub_f32_e32 v64, v56, v252
	v_sub_f32_e32 v65, v57, v253
	v_lshlrev_b32_e32 v252, 16, v194
	v_and_b32_e32 v253, 0xffff0000, v194
	v_sub_f32_e32 v66, v58, v252
	v_sub_f32_e32 v67, v59, v253
	v_lshlrev_b32_e32 v252, 16, v195
	v_and_b32_e32 v253, 0xffff0000, v195
	v_sub_f32_e32 v68, v60, v252
	v_sub_f32_e32 v69, v61, v253
	v_cvt_pk_bf16_f32 v248, v62, v63
	v_cvt_pk_bf16_f32 v249, v64, v65
	v_cvt_pk_bf16_f32 v250, v66, v67
	v_cvt_pk_bf16_f32 v251, v68, v69
	s_nop 1
	v_mfma_f32_32x32x16_bf16 v[2:17], v[248:251], v[116:119], v[2:17]
	v_mfma_f32_32x32x16_bf16 v[18:33], v[248:251], v[120:123], v[18:33]
	s_waitcnt lgkmcnt(0)
	ds_read_b128 v[200:203], v111 offset:896
	ds_read_b128 v[204:207], v111 offset:912
	ds_read_b128 v[208:211], v111 offset:1920
	ds_read_b128 v[212:215], v111 offset:1936
	ds_read_b128 v[216:219], v111 offset:2944
	ds_read_b128 v[220:223], v111 offset:2960
	s_waitcnt vmcnt(13)
	v_lshlrev_b32_e32 v54, 16, v132
	v_and_b32_e32 v55, 0xffff0000, v132
	v_lshlrev_b32_e32 v56, 16, v133
	v_and_b32_e32 v57, 0xffff0000, v133
	v_lshlrev_b32_e32 v58, 16, v134
	v_and_b32_e32 v59, 0xffff0000, v134
	v_lshlrev_b32_e32 v60, 16, v135
	v_and_b32_e32 v61, 0xffff0000, v135
	v_pk_mul_f32 v[54:55], v[46:47], v[54:55]
	v_pk_mul_f32 v[56:57], v[46:47], v[56:57]
	v_pk_mul_f32 v[58:59], v[46:47], v[58:59]
	v_pk_mul_f32 v[60:61], v[46:47], v[60:61]
	v_pk_mul_f32 v[54:55], v[224:225], v[54:55]
	v_pk_mul_f32 v[56:57], v[226:227], v[56:57]
	v_pk_mul_f32 v[58:59], v[228:229], v[58:59]
	v_pk_mul_f32 v[60:61], v[230:231], v[60:61]
	v_pk_fma_f32 v[54:55], v[232:233], v[54:55], v[240:241]
	v_pk_fma_f32 v[56:57], v[234:235], v[56:57], v[242:243]
	v_pk_fma_f32 v[58:59], v[236:237], v[58:59], v[244:245]
	v_pk_fma_f32 v[60:61], v[238:239], v[60:61], v[246:247]
	v_med3_f32 v62, v54, s82, v108
	v_med3_f32 v63, v55, s82, v108
	v_med3_f32 v64, v56, s82, v108
	v_med3_f32 v65, v57, s82, v108
	v_med3_f32 v66, v58, s82, v108
	v_med3_f32 v67, v59, s82, v108
	v_med3_f32 v68, v60, s82, v108
	v_med3_f32 v69, v61, s82, v108
	v_cvt_pk_bf16_f32 v192, v54, v55
	v_cvt_pk_bf16_f32 v193, v56, v57
	v_cvt_pk_bf16_f32 v194, v58, v59
	v_cvt_pk_bf16_f32 v195, v60, v61
	v_cvt_pk_fp8_f32 v70, v62, v63
	v_cvt_pk_fp8_f32 v71, v66, v67
	v_cvt_pk_fp8_f32 v70, v64, v65 op_sel:[0,0,1]
	v_cvt_pk_fp8_f32 v71, v68, v69 op_sel:[0,0,1]
	s_nop 0
	global_store_dwordx2 v[72:73], v[70:71], off offset:208
	v_mfma_f32_32x32x16_bf16 v[2:17], v[192:195], v[136:139], v[2:17]
	v_mfma_f32_32x32x16_bf16 v[18:33], v[192:195], v[140:143], v[18:33]
	v_mfma_f32_32x32x16_bf16 v[2:17], v[192:195], v[144:147], v[2:17]
	v_mfma_f32_32x32x16_bf16 v[18:33], v[192:195], v[148:151], v[18:33]
	v_lshlrev_b32_e32 v252, 16, v192
	v_and_b32_e32 v253, 0xffff0000, v192
	v_sub_f32_e32 v62, v54, v252
	v_sub_f32_e32 v63, v55, v253
	v_lshlrev_b32_e32 v252, 16, v193
	v_and_b32_e32 v253, 0xffff0000, v193
	v_sub_f32_e32 v64, v56, v252
	v_sub_f32_e32 v65, v57, v253
	v_lshlrev_b32_e32 v252, 16, v194
	v_and_b32_e32 v253, 0xffff0000, v194
	v_sub_f32_e32 v66, v58, v252
	v_sub_f32_e32 v67, v59, v253
	v_lshlrev_b32_e32 v252, 16, v195
	v_and_b32_e32 v253, 0xffff0000, v195
	v_sub_f32_e32 v68, v60, v252
	v_sub_f32_e32 v69, v61, v253
	v_cvt_pk_bf16_f32 v248, v62, v63
	v_cvt_pk_bf16_f32 v249, v64, v65
	v_cvt_pk_bf16_f32 v250, v66, v67
	v_cvt_pk_bf16_f32 v251, v68, v69
	s_nop 1
	v_mfma_f32_32x32x16_bf16 v[2:17], v[248:251], v[136:139], v[2:17]
	v_mfma_f32_32x32x16_bf16 v[18:33], v[248:251], v[140:143], v[18:33]
	s_waitcnt lgkmcnt(0)
	ds_read_b128 v[224:227], v111 offset:960
	ds_read_b128 v[228:231], v111 offset:976
	ds_read_b128 v[232:235], v111 offset:1984
	ds_read_b128 v[236:239], v111 offset:2000
	ds_read_b128 v[240:243], v111 offset:3008
	ds_read_b128 v[244:247], v111 offset:3024
	s_waitcnt vmcnt(8)
	v_lshlrev_b32_e32 v54, 16, v152
	v_and_b32_e32 v55, 0xffff0000, v152
	v_lshlrev_b32_e32 v56, 16, v153
	v_and_b32_e32 v57, 0xffff0000, v153
	v_lshlrev_b32_e32 v58, 16, v154
	v_and_b32_e32 v59, 0xffff0000, v154
	v_lshlrev_b32_e32 v60, 16, v155
	v_and_b32_e32 v61, 0xffff0000, v155
	v_pk_mul_f32 v[54:55], v[46:47], v[54:55]
	v_pk_mul_f32 v[56:57], v[46:47], v[56:57]
	v_pk_mul_f32 v[58:59], v[46:47], v[58:59]
	v_pk_mul_f32 v[60:61], v[46:47], v[60:61]
	v_pk_mul_f32 v[54:55], v[200:201], v[54:55]
	v_pk_mul_f32 v[56:57], v[202:203], v[56:57]
	v_pk_mul_f32 v[58:59], v[204:205], v[58:59]
	v_pk_mul_f32 v[60:61], v[206:207], v[60:61]
	v_pk_fma_f32 v[54:55], v[208:209], v[54:55], v[216:217]
	v_pk_fma_f32 v[56:57], v[210:211], v[56:57], v[218:219]
	v_pk_fma_f32 v[58:59], v[212:213], v[58:59], v[220:221]
	v_pk_fma_f32 v[60:61], v[214:215], v[60:61], v[222:223]
	v_med3_f32 v62, v54, s82, v108
	v_med3_f32 v63, v55, s82, v108
	v_med3_f32 v64, v56, s82, v108
	v_med3_f32 v65, v57, s82, v108
	v_med3_f32 v66, v58, s82, v108
	v_med3_f32 v67, v59, s82, v108
	v_med3_f32 v68, v60, s82, v108
	v_med3_f32 v69, v61, s82, v108
	v_cvt_pk_bf16_f32 v192, v54, v55
	v_cvt_pk_bf16_f32 v193, v56, v57
	v_cvt_pk_bf16_f32 v194, v58, v59
	v_cvt_pk_bf16_f32 v195, v60, v61
	v_cvt_pk_fp8_f32 v70, v62, v63
	v_cvt_pk_fp8_f32 v71, v66, v67
	v_cvt_pk_fp8_f32 v70, v64, v65 op_sel:[0,0,1]
	v_cvt_pk_fp8_f32 v71, v68, v69 op_sel:[0,0,1]
	s_nop 0
	global_store_dwordx2 v[72:73], v[70:71], off offset:224
	v_mfma_f32_32x32x16_bf16 v[2:17], v[192:195], v[156:159], v[2:17]
	v_mfma_f32_32x32x16_bf16 v[18:33], v[192:195], v[160:163], v[18:33]
	v_mfma_f32_32x32x16_bf16 v[2:17], v[192:195], v[164:167], v[2:17]
	v_mfma_f32_32x32x16_bf16 v[18:33], v[192:195], v[168:171], v[18:33]
	v_lshlrev_b32_e32 v252, 16, v192
	v_and_b32_e32 v253, 0xffff0000, v192
	v_sub_f32_e32 v62, v54, v252
	v_sub_f32_e32 v63, v55, v253
	v_lshlrev_b32_e32 v252, 16, v193
	v_and_b32_e32 v253, 0xffff0000, v193
	v_sub_f32_e32 v64, v56, v252
	v_sub_f32_e32 v65, v57, v253
	v_lshlrev_b32_e32 v252, 16, v194
	v_and_b32_e32 v253, 0xffff0000, v194
	v_sub_f32_e32 v66, v58, v252
	v_sub_f32_e32 v67, v59, v253
	v_lshlrev_b32_e32 v252, 16, v195
	v_and_b32_e32 v253, 0xffff0000, v195
	v_sub_f32_e32 v68, v60, v252
	v_sub_f32_e32 v69, v61, v253
	v_cvt_pk_bf16_f32 v248, v62, v63
	v_cvt_pk_bf16_f32 v249, v64, v65
	v_cvt_pk_bf16_f32 v250, v66, v67
	v_cvt_pk_bf16_f32 v251, v68, v69
	s_nop 1
	v_mfma_f32_32x32x16_bf16 v[2:17], v[248:251], v[156:159], v[2:17]
	v_mfma_f32_32x32x16_bf16 v[18:33], v[248:251], v[160:163], v[18:33]
	s_waitcnt lgkmcnt(0)
	s_waitcnt vmcnt(3)
	v_lshlrev_b32_e32 v54, 16, v172
	v_and_b32_e32 v55, 0xffff0000, v172
	v_lshlrev_b32_e32 v56, 16, v173
	v_and_b32_e32 v57, 0xffff0000, v173
	v_lshlrev_b32_e32 v58, 16, v174
	v_and_b32_e32 v59, 0xffff0000, v174
	v_lshlrev_b32_e32 v60, 16, v175
	v_and_b32_e32 v61, 0xffff0000, v175
	v_pk_mul_f32 v[54:55], v[46:47], v[54:55]
	v_pk_mul_f32 v[56:57], v[46:47], v[56:57]
	v_pk_mul_f32 v[58:59], v[46:47], v[58:59]
	v_pk_mul_f32 v[60:61], v[46:47], v[60:61]
	v_pk_mul_f32 v[54:55], v[224:225], v[54:55]
	v_pk_mul_f32 v[56:57], v[226:227], v[56:57]
	v_pk_mul_f32 v[58:59], v[228:229], v[58:59]
	v_pk_mul_f32 v[60:61], v[230:231], v[60:61]
	v_pk_fma_f32 v[54:55], v[232:233], v[54:55], v[240:241]
	v_pk_fma_f32 v[56:57], v[234:235], v[56:57], v[242:243]
	v_pk_fma_f32 v[58:59], v[236:237], v[58:59], v[244:245]
	v_pk_fma_f32 v[60:61], v[238:239], v[60:61], v[246:247]
	v_med3_f32 v62, v54, s82, v108
	v_med3_f32 v63, v55, s82, v108
	v_med3_f32 v64, v56, s82, v108
	v_med3_f32 v65, v57, s82, v108
	v_med3_f32 v66, v58, s82, v108
	v_med3_f32 v67, v59, s82, v108
	v_med3_f32 v68, v60, s82, v108
	v_med3_f32 v69, v61, s82, v108
	v_cvt_pk_bf16_f32 v192, v54, v55
	v_cvt_pk_bf16_f32 v193, v56, v57
	v_cvt_pk_bf16_f32 v194, v58, v59
	v_cvt_pk_bf16_f32 v195, v60, v61
	v_cvt_pk_fp8_f32 v70, v62, v63
	v_cvt_pk_fp8_f32 v71, v66, v67
	v_cvt_pk_fp8_f32 v70, v64, v65 op_sel:[0,0,1]
	v_cvt_pk_fp8_f32 v71, v68, v69 op_sel:[0,0,1]
	s_nop 0
	global_store_dwordx2 v[72:73], v[70:71], off offset:240
	v_mfma_f32_32x32x16_bf16 v[2:17], v[192:195], v[176:179], v[2:17]
	v_mfma_f32_32x32x16_bf16 v[18:33], v[192:195], v[180:183], v[18:33]
	v_mfma_f32_32x32x16_bf16 v[2:17], v[192:195], v[184:187], v[2:17]
	v_mfma_f32_32x32x16_bf16 v[18:33], v[192:195], v[188:191], v[18:33]
	v_lshlrev_b32_e32 v252, 16, v192
	v_and_b32_e32 v253, 0xffff0000, v192
	v_sub_f32_e32 v62, v54, v252
	v_sub_f32_e32 v63, v55, v253
	v_lshlrev_b32_e32 v252, 16, v193
	v_and_b32_e32 v253, 0xffff0000, v193
	v_sub_f32_e32 v64, v56, v252
	v_sub_f32_e32 v65, v57, v253
	v_lshlrev_b32_e32 v252, 16, v194
	v_and_b32_e32 v253, 0xffff0000, v194
	v_sub_f32_e32 v66, v58, v252
	v_sub_f32_e32 v67, v59, v253
	v_lshlrev_b32_e32 v252, 16, v195
	v_and_b32_e32 v253, 0xffff0000, v195
	v_sub_f32_e32 v68, v60, v252
	v_sub_f32_e32 v69, v61, v253
	v_cvt_pk_bf16_f32 v248, v62, v63
	v_cvt_pk_bf16_f32 v249, v64, v65
	v_cvt_pk_bf16_f32 v250, v66, v67
	v_cvt_pk_bf16_f32 v251, v68, v69
	s_nop 1
	v_mfma_f32_32x32x16_bf16 v[2:17], v[248:251], v[176:179], v[2:17]
	v_mfma_f32_32x32x16_bf16 v[18:33], v[248:251], v[180:183], v[18:33]
	v_and_b32_e32 v62, 0xffffff00, v103
	v_lshlrev_b32_e32 v62, 6, v62
	v_lshl_add_u32 v62, v254, 4, v62
	v_lshlrev_b32_e32 v63, 12, v75
	v_sub_u32_e32 v62, v62, v63
	v_add_u32_e32 v62, 0x3000, v62
	v_sub_u32_e32 v62, 0, v62
	v_ashrrev_i32_e32 v63, 31, v62
	v_lshl_add_u64 v[34:35], v[34:35], 0, v[62:63]
	v_lshl_add_u64 v[36:37], v[36:37], 0, v[62:63]
	v_lshl_add_u64 v[38:39], v[38:39], 0, v[62:63]
	v_lshl_add_u64 v[40:41], v[40:41], 0, v[62:63]
	s_nop 7
	v_add_u32_e32 v1, 0x400, v83
	s_nop 9
	ds_write2_b32 v1, v2, v18 offset1:32
	ds_write2_b32 v1, v3, v19 offset0:64 offset1:96
	ds_write2_b32 v1, v4, v20 offset0:128 offset1:160
	ds_write2_b32 v1, v5, v21 offset0:192 offset1:224
	v_add_u32_e32 v1, 0xc00, v83
	ds_write2_b32 v1, v6, v22 offset1:32
	ds_write2_b32 v1, v7, v23 offset0:64 offset1:96
	ds_write2_b32 v1, v8, v24 offset0:128 offset1:160
	ds_write2_b32 v1, v9, v25 offset0:192 offset1:224
	v_add_u32_e32 v1, 0x1400, v83
	ds_write2_b32 v1, v10, v26 offset1:32
	ds_write2_b32 v1, v11, v27 offset0:64 offset1:96
	ds_write2_b32 v1, v12, v28 offset0:128 offset1:160
	ds_write2_b32 v1, v13, v29 offset0:192 offset1:224
	v_add_u32_e32 v1, 0x1c00, v83
	ds_write2_b32 v1, v14, v30 offset1:32
	ds_write2_b32 v1, v15, v31 offset0:64 offset1:96
	ds_write2_b32 v1, v16, v32 offset0:128 offset1:160
	ds_write2_b32 v1, v17, v33 offset0:192 offset1:224
	s_waitcnt lgkmcnt(0)
	s_barrier
	global_load_dword v1, v[42:43], off
	v_add_u32_e32 v8, s66, v84
	ds_read2st64_b32 v[2:3], v8 offset0:4 offset1:36
	ds_read2st64_b32 v[4:5], v8 offset0:68 offset1:100
	ds_read2st64_b32 v[6:7], v8 offset0:132 offset1:164
	ds_read2st64_b32 v[8:9], v8 offset0:196 offset1:228
	s_waitcnt lgkmcnt(3)
	v_add_f32_e32 v2, 0, v2
	v_add_f32_e32 v2, v2, v3
	s_waitcnt lgkmcnt(2)
	v_add_f32_e32 v2, v2, v4
	v_add_f32_e32 v2, v2, v5
	s_waitcnt lgkmcnt(1)
	v_add_f32_e32 v2, v2, v6
	v_add_f32_e32 v2, v2, v7
	s_waitcnt lgkmcnt(0)
	v_add_f32_e32 v2, v2, v8
	v_add_f32_e32 v2, v2, v9
	v_mul_f32_e32 v3, 0xbfb8aa3b, v2
	v_fma_f32 v4, v2, s83, -v3
	v_rndne_f32_e32 v5, v3
	v_fmac_f32_e32 v4, 0xb2a5705f, v2
	v_sub_f32_e32 v3, v3, v5
	v_add_f32_e32 v3, v3, v4
	v_cvt_i32_f32_e32 v5, v5
	v_exp_f32_e32 v3, v3
	v_cmp_nlt_f32_e32 vcc, s84, v2
	v_ldexp_f32 v3, v3, v5
	s_nop 0
	v_cndmask_b32_e32 v3, 0, v3, vcc
	v_cmp_ngt_f32_e32 vcc, s85, v2
	s_nop 1
	v_cndmask_b32_e32 v2, v109, v3, vcc
	v_add_f32_e32 v2, 1.0, v2
	v_div_scale_f32 v3, s[34:35], v2, v2, 1.0
	v_rcp_f32_e32 v4, v3
	v_div_scale_f32 v5, vcc, 1.0, v2, 1.0
	v_fma_f32 v6, -v3, v4, 1.0
	v_fmac_f32_e32 v4, v6, v4
	v_mul_f32_e32 v6, v5, v4
	v_fma_f32 v7, -v3, v6, v5
	v_fmac_f32_e32 v6, v7, v4
	v_fma_f32 v3, -v3, v6, v5
	v_div_fmas_f32 v3, v3, v4, v6
	v_div_fixup_f32 v2, v3, v2, 1.0
	s_waitcnt vmcnt(0)
	v_mov_b32_e32 v128, v1
	v_add_f32_e32 v1, v1, v2
	ds_bpermute_b32 v3, v88, v1
	ds_bpermute_b32 v4, v89, v1
	ds_bpermute_b32 v5, v90, v1
	ds_bpermute_b32 v6, v91, v1
	ds_bpermute_b32 v7, v92, v1
	s_waitcnt lgkmcnt(4)
	v_cmp_eq_f32_e64 s[34:35], v1, v3
	v_cmp_lt_f32_e32 vcc, v1, v3
	s_waitcnt lgkmcnt(3)
	v_cmp_eq_f32_e64 s[38:39], v1, v4
	s_and_b64 s[34:35], s[4:5], s[34:35]
	v_cmp_lt_f32_e64 s[36:37], v1, v4
	s_waitcnt lgkmcnt(2)
	v_cmp_eq_f32_e64 s[42:43], v1, v5
	s_and_b64 s[38:39], s[6:7], s[38:39]
	s_or_b64 s[34:35], vcc, s[34:35]
	v_cmp_lt_f32_e64 s[40:41], v1, v5
	s_waitcnt lgkmcnt(1)
	v_cmp_eq_f32_e64 s[46:47], v1, v6
	s_and_b64 s[42:43], s[8:9], s[42:43]
	v_cndmask_b32_e64 v3, 0, 1, s[34:35]
	s_or_b64 s[34:35], s[36:37], s[38:39]
	v_cmp_lt_f32_e64 s[44:45], v1, v6
	s_and_b64 s[46:47], s[10:11], s[46:47]
	v_cndmask_b32_e64 v4, 0, 1, s[34:35]
	s_or_b64 s[34:35], s[40:41], s[42:43]
	v_cndmask_b32_e64 v5, 0, 1, s[34:35]
	s_or_b64 s[34:35], s[44:45], s[46:47]
	v_add3_u32 v3, v3, v4, v5
	v_cndmask_b32_e64 v4, 0, 1, s[34:35]
	s_waitcnt lgkmcnt(0)
	v_cmp_eq_f32_e64 s[34:35], v1, v7
	v_cmp_lt_f32_e32 vcc, v1, v7
	ds_bpermute_b32 v5, v93, v1
	s_and_b64 s[34:35], s[12:13], s[34:35]
	s_or_b64 s[34:35], vcc, s[34:35]
	v_cndmask_b32_e64 v6, 0, 1, s[34:35]
	v_add3_u32 v3, v3, v4, v6
	ds_bpermute_b32 v4, v94, v1
	s_waitcnt lgkmcnt(1)
	v_cmp_eq_f32_e64 s[34:35], v1, v5
	ds_bpermute_b32 v6, v95, v1
	v_cmp_lt_f32_e32 vcc, v1, v5
	s_and_b64 s[34:35], s[14:15], s[34:35]
	s_or_b64 s[34:35], vcc, s[34:35]
	v_cndmask_b32_e64 v5, 0, 1, s[34:35]
	s_waitcnt lgkmcnt(1)
	v_cmp_eq_f32_e64 s[34:35], v1, v4
	v_cmp_lt_f32_e32 vcc, v1, v4
	s_and_b64 s[34:35], s[16:17], s[34:35]
	s_or_b64 s[34:35], vcc, s[34:35]
	s_waitcnt lgkmcnt(0)
	v_cmp_lt_f32_e32 vcc, v1, v6
	v_cndmask_b32_e64 v4, 0, 1, s[34:35]
	s_mov_b32 s40, 0
	v_addc_co_u32_e32 v3, vcc, v3, v5, vcc
	v_add_u32_e32 v3, v3, v4
	v_cmp_gt_u32_e32 vcc, 2, v3
	s_nop 1
	v_cndmask_b32_e32 v3, 0, v1, vcc
	s_waitcnt lgkmcnt(0)
	s_nop 1
	v_add_f32_dpp v3, v3, v3 quad_perm:[1,0,3,2] row_mask:0xf bank_mask:0xf
	s_waitcnt lgkmcnt(0)
	s_nop 1
	v_add_f32_dpp v3, v3, v3 quad_perm:[2,3,0,1] row_mask:0xf bank_mask:0xf
	s_waitcnt lgkmcnt(0)
	s_nop 1
	v_add_f32_dpp v3, v3, v3 row_half_mirror row_mask:0xf bank_mask:0xf
	ds_bpermute_b32 v4, v87, v3
	ds_bpermute_b32 v5, v96, v3
	ds_bpermute_b32 v6, v97, v3
	ds_bpermute_b32 v7, v98, v3
	ds_bpermute_b32 v8, v99, v3
	s_waitcnt lgkmcnt(4)
	v_cmp_eq_f32_e64 s[34:35], v3, v4
	v_cmp_lt_f32_e32 vcc, v3, v4
	s_and_b64 s[34:35], s[18:19], s[34:35]
	s_or_b64 s[34:35], vcc, s[34:35]
	v_cndmask_b32_e64 v4, 0, 1, s[34:35]
	s_waitcnt lgkmcnt(3)
	v_cmp_eq_f32_e64 s[34:35], v3, v5
	v_cmp_lt_f32_e32 vcc, v3, v5
	s_and_b64 s[34:35], s[20:21], s[34:35]
	s_or_b64 s[34:35], vcc, s[34:35]
	v_cndmask_b32_e64 v5, 0, 1, s[34:35]
	s_waitcnt lgkmcnt(2)
	v_cmp_eq_f32_e64 s[34:35], v3, v6
	v_cmp_lt_f32_e32 vcc, v3, v6
	s_and_b64 s[34:35], s[22:23], s[34:35]
	s_or_b64 s[34:35], vcc, s[34:35]
	v_cndmask_b32_e64 v6, 0, 1, s[34:35]
	s_waitcnt lgkmcnt(1)
	v_cmp_eq_f32_e64 s[34:35], v3, v7
	v_cmp_lt_f32_e32 vcc, v3, v7
	s_and_b64 s[34:35], s[24:25], s[34:35]
	ds_bpermute_b32 v9, v100, v3
	s_or_b64 s[34:35], vcc, s[34:35]
	v_cndmask_b32_e64 v7, 0, 1, s[34:35]
	s_waitcnt lgkmcnt(1)
	v_cmp_eq_f32_e64 s[34:35], v3, v8
	v_cmp_lt_f32_e32 vcc, v3, v8
	s_and_b64 s[34:35], s[26:27], s[34:35]
	ds_bpermute_b32 v10, v101, v3
	s_or_b64 s[34:35], vcc, s[34:35]
	v_cndmask_b32_e64 v8, 0, 1, s[34:35]
	s_waitcnt lgkmcnt(1)
	v_cmp_eq_f32_e64 s[34:35], v3, v9
	ds_bpermute_b32 v11, v102, v3
	v_cmp_lt_f32_e32 vcc, v3, v9
	s_and_b64 s[34:35], s[28:29], s[34:35]
	s_or_b64 s[34:35], vcc, s[34:35]
	v_cndmask_b32_e64 v9, 0, 1, s[34:35]
	s_waitcnt lgkmcnt(1)
	v_cmp_eq_f32_e64 s[34:35], v3, v10
	v_cmp_lt_f32_e32 vcc, v3, v10
	s_and_b64 s[34:35], s[30:31], s[34:35]
	s_or_b64 s[34:35], vcc, s[34:35]
	s_waitcnt lgkmcnt(0)
	v_cmp_lt_f32_e32 vcc, v3, v11
	v_cndmask_b32_e64 v10, 0, 1, s[34:35]
	s_nop 0
	v_cndmask_b32_e64 v3, 0, 1, vcc
	v_add_u32_e32 v3, v5, v3
	v_add3_u32 v3, v3, v4, v6
	v_add3_u32 v3, v3, v7, v8
	v_add3_u32 v3, v3, v9, v10
	v_cmp_gt_u32_e32 vcc, 4, v3
	v_mov_b32_e32 v5, 0
	v_mov_b32_e32 v4, v104
	v_cndmask_b32_e32 v3, v110, v1, vcc

.LBB0_1889:
	s_or_b64 exec, exec, s[34:35]
	v_add_u32_e32 v1, s72, v84
	ds_read2st64_b32 v[2:3], v1 offset0:4 offset1:36
	s_mov_b32 s41, 0
	s_waitcnt lgkmcnt(0)
	v_add_f32_e32 v2, 0, v2
	v_add_f32_e32 v4, v2, v3
	ds_read2st64_b32 v[2:3], v1 offset0:68 offset1:100
	s_waitcnt lgkmcnt(0)
	v_add_f32_e32 v2, v4, v2
	v_add_f32_e32 v4, v2, v3
	ds_read2st64_b32 v[2:3], v1 offset0:132 offset1:164
	s_waitcnt lgkmcnt(0)
	v_add_f32_e32 v2, v4, v2
	v_add_f32_e32 v4, v2, v3
	ds_read2st64_b32 v[2:3], v1 offset0:196 offset1:228
	s_waitcnt lgkmcnt(0)
	v_add_f32_e32 v1, v4, v2
	v_add_f32_e32 v1, v1, v3
	v_mul_f32_e32 v2, 0xbfb8aa3b, v1
	v_fma_f32 v3, v1, s83, -v2
	v_rndne_f32_e32 v4, v2
	v_fmac_f32_e32 v3, 0xb2a5705f, v1
	v_sub_f32_e32 v2, v2, v4
	v_add_f32_e32 v2, v2, v3
	v_exp_f32_e32 v2, v2
	v_cvt_i32_f32_e32 v3, v4
	v_cmp_nlt_f32_e32 vcc, s84, v1
	v_ldexp_f32 v2, v2, v3
	s_nop 0
	v_cndmask_b32_e32 v2, 0, v2, vcc
	v_cmp_ngt_f32_e32 vcc, s85, v1
	s_nop 1
	v_cndmask_b32_e32 v1, v109, v2, vcc
	v_add_f32_e32 v1, 1.0, v1
	v_div_scale_f32 v2, s[34:35], v1, v1, 1.0
	v_rcp_f32_e32 v3, v2
	s_nop 0
	v_fma_f32 v4, -v2, v3, 1.0
	v_fmac_f32_e32 v3, v4, v3
	v_div_scale_f32 v4, vcc, 1.0, v1, 1.0
	v_mul_f32_e32 v5, v4, v3
	v_fma_f32 v6, -v2, v5, v4
	v_fmac_f32_e32 v5, v6, v3
	v_fma_f32 v2, -v2, v5, v4
	v_div_fmas_f32 v2, v2, v3, v5
	v_div_fixup_f32 v2, v2, v1, 1.0
	v_mov_b32_e32 v1, v128
	v_add_f32_e32 v3, v1, v2
	ds_bpermute_b32 v1, v88, v3
	ds_bpermute_b32 v4, v89, v3
	ds_bpermute_b32 v5, v90, v3
	ds_bpermute_b32 v6, v95, v3
	s_waitcnt lgkmcnt(3)
	v_cmp_eq_f32_e64 s[34:35], v3, v1
	v_cmp_lt_f32_e32 vcc, v3, v1
	s_and_b64 s[34:35], s[4:5], s[34:35]
	s_or_b64 s[34:35], vcc, s[34:35]
	v_cndmask_b32_e64 v1, 0, 1, s[34:35]
	s_waitcnt lgkmcnt(2)
	v_cmp_eq_f32_e64 s[34:35], v3, v4
	v_cmp_lt_f32_e32 vcc, v3, v4
	s_and_b64 s[34:35], s[6:7], s[34:35]
	s_or_b64 s[34:35], vcc, s[34:35]
	v_cndmask_b32_e64 v4, 0, 1, s[34:35]
	s_waitcnt lgkmcnt(1)
	v_cmp_eq_f32_e64 s[34:35], v3, v5
	v_cmp_lt_f32_e32 vcc, v3, v5
	s_and_b64 s[34:35], s[8:9], s[34:35]
	s_or_b64 s[34:35], vcc, s[34:35]
	v_cndmask_b32_e64 v5, 0, 1, s[34:35]
	v_add3_u32 v1, v1, v4, v5
	ds_bpermute_b32 v4, v91, v3
	ds_bpermute_b32 v5, v92, v3
	s_waitcnt lgkmcnt(1)
	v_cmp_eq_f32_e64 s[34:35], v3, v4
	v_cmp_lt_f32_e32 vcc, v3, v4
	s_and_b64 s[34:35], s[10:11], s[34:35]
	s_or_b64 s[34:35], vcc, s[34:35]
	v_cndmask_b32_e64 v4, 0, 1, s[34:35]
	s_waitcnt lgkmcnt(0)
	v_cmp_eq_f32_e64 s[34:35], v3, v5
	v_cmp_lt_f32_e32 vcc, v3, v5
	s_and_b64 s[34:35], s[12:13], s[34:35]
	s_or_b64 s[34:35], vcc, s[34:35]
	v_cndmask_b32_e64 v5, 0, 1, s[34:35]
	v_add3_u32 v1, v1, v4, v5
	ds_bpermute_b32 v4, v93, v3
	ds_bpermute_b32 v5, v94, v3
	s_waitcnt lgkmcnt(1)
	v_cmp_eq_f32_e64 s[34:35], v3, v4
	v_cmp_lt_f32_e32 vcc, v3, v4
	s_and_b64 s[34:35], s[14:15], s[34:35]
	s_or_b64 s[34:35], vcc, s[34:35]
	v_cndmask_b32_e64 v4, 0, 1, s[34:35]
	s_waitcnt lgkmcnt(0)
	v_cmp_eq_f32_e64 s[34:35], v3, v5
	v_cmp_lt_f32_e32 vcc, v3, v5
	s_and_b64 s[34:35], s[16:17], s[34:35]
	s_or_b64 s[34:35], vcc, s[34:35]
	v_cmp_lt_f32_e32 vcc, v3, v6
	v_cndmask_b32_e64 v5, 0, 1, s[34:35]
	s_nop 0
	v_addc_co_u32_e32 v1, vcc, v1, v4, vcc
	v_add_u32_e32 v1, v1, v5
	v_cmp_gt_u32_e32 vcc, 2, v1
	s_nop 1
	v_cndmask_b32_e32 v1, 0, v3, vcc
	s_waitcnt lgkmcnt(0)
	s_nop 1
	v_add_f32_dpp v1, v1, v1 quad_perm:[1,0,3,2] row_mask:0xf bank_mask:0xf
	s_waitcnt lgkmcnt(0)
	s_nop 1
	v_add_f32_dpp v1, v1, v1 quad_perm:[2,3,0,1] row_mask:0xf bank_mask:0xf
	s_waitcnt lgkmcnt(0)
	s_nop 1
	v_add_f32_dpp v1, v1, v1 row_half_mirror row_mask:0xf bank_mask:0xf
	ds_bpermute_b32 v4, v87, v1
	ds_bpermute_b32 v5, v96, v1
	ds_bpermute_b32 v6, v97, v1
	ds_bpermute_b32 v7, v98, v1
	ds_bpermute_b32 v8, v99, v1
	s_waitcnt lgkmcnt(4)
	v_cmp_eq_f32_e64 s[34:35], v1, v4
	v_cmp_lt_f32_e32 vcc, v1, v4
	s_and_b64 s[34:35], s[18:19], s[34:35]
	s_or_b64 s[34:35], vcc, s[34:35]
	v_cndmask_b32_e64 v4, 0, 1, s[34:35]
	s_waitcnt lgkmcnt(3)
	v_cmp_eq_f32_e64 s[34:35], v1, v5
	v_cmp_lt_f32_e32 vcc, v1, v5
	s_and_b64 s[34:35], s[20:21], s[34:35]
	s_or_b64 s[34:35], vcc, s[34:35]
	v_cndmask_b32_e64 v5, 0, 1, s[34:35]
	s_waitcnt lgkmcnt(2)
	v_cmp_eq_f32_e64 s[34:35], v1, v6
	v_cmp_lt_f32_e32 vcc, v1, v6
	s_and_b64 s[34:35], s[22:23], s[34:35]
	s_or_b64 s[34:35], vcc, s[34:35]
	v_cndmask_b32_e64 v6, 0, 1, s[34:35]
	s_waitcnt lgkmcnt(1)
	v_cmp_eq_f32_e64 s[34:35], v1, v7
	v_cmp_lt_f32_e32 vcc, v1, v7
	s_and_b64 s[34:35], s[24:25], s[34:35]
	ds_bpermute_b32 v9, v100, v1
	s_or_b64 s[34:35], vcc, s[34:35]
	v_cndmask_b32_e64 v7, 0, 1, s[34:35]
	s_waitcnt lgkmcnt(1)
	v_cmp_eq_f32_e64 s[34:35], v1, v8
	v_cmp_lt_f32_e32 vcc, v1, v8
	s_and_b64 s[34:35], s[26:27], s[34:35]
	ds_bpermute_b32 v10, v101, v1
	s_or_b64 s[34:35], vcc, s[34:35]
	v_cndmask_b32_e64 v8, 0, 1, s[34:35]
	s_waitcnt lgkmcnt(1)
	v_cmp_eq_f32_e64 s[34:35], v1, v9
	ds_bpermute_b32 v11, v102, v1
	v_cmp_lt_f32_e32 vcc, v1, v9
	s_and_b64 s[34:35], s[28:29], s[34:35]
	s_or_b64 s[34:35], vcc, s[34:35]
	v_cndmask_b32_e64 v9, 0, 1, s[34:35]
	s_waitcnt lgkmcnt(1)
	v_cmp_eq_f32_e64 s[34:35], v1, v10
	v_cmp_lt_f32_e32 vcc, v1, v10
	s_and_b64 s[34:35], s[30:31], s[34:35]
	s_or_b64 s[34:35], vcc, s[34:35]
	s_waitcnt lgkmcnt(0)
	v_cmp_lt_f32_e32 vcc, v1, v11
	v_cndmask_b32_e64 v10, 0, 1, s[34:35]
	s_nop 0
	v_cndmask_b32_e64 v1, 0, 1, vcc
	v_add_u32_e32 v1, v5, v1
	v_add3_u32 v1, v1, v4, v6
	v_add3_u32 v1, v1, v7, v8
	v_add3_u32 v1, v1, v9, v10
	v_cmp_gt_u32_e32 vcc, 4, v1
	v_mov_b32_e32 v5, 0
	v_mov_b32_e32 v4, v104
	v_cndmask_b32_e32 v3, v110, v3, vcc

.Lrk_exit_1:
	v_cmp_gt_u32_e64 s[34:35], 8, v5
	s_and_b64 vcc, vcc, s[34:35]
	v_cndmask_b32_e32 v1, 0, v2, vcc
	s_waitcnt lgkmcnt(0)
	s_nop 1
	v_add_f32_dpp v1, v1, v1 quad_perm:[1,0,3,2] row_mask:0xf bank_mask:0xf
	s_waitcnt lgkmcnt(0)
	s_nop 1
	v_add_f32_dpp v1, v1, v1 quad_perm:[2,3,0,1] row_mask:0xf bank_mask:0xf
	s_waitcnt lgkmcnt(0)
	s_nop 1
	v_add_f32_dpp v1, v1, v1 row_half_mirror row_mask:0xf bank_mask:0xf
	s_waitcnt lgkmcnt(0)
	s_nop 1
	v_add_f32_dpp v1, v1, v1 row_mirror row_mask:0xf bank_mask:0xf
	s_waitcnt lgkmcnt(0)
	v_mov_b32_e32 v3, v1
	s_nop 1
	v_permlane16_swap_b32_e32 v3, v1
	v_add_f32_e32 v3, v1, v3
	ds_bpermute_b32 v4, v81, v3
	s_and_saveexec_b64 s[34:35], vcc
	s_cbranch_execz .LBB0_1893
	s_add_i32 s36, s69, s87
	s_waitcnt lgkmcnt(0)
	v_add_f32_e32 v1, v3, v4
	v_lshl_or_b32 v6, s36, 3, v5
	v_div_scale_f32 v3, s[36:37], v1, v1, v2
	v_rcp_f32_e32 v10, v3
	v_ashrrev_i32_e32 v7, 31, v6
	v_lshlrev_b64 v[6:7], 2, v[6:7]
	v_lshl_add_u64 v[8:9], s[56:57], 0, v[6:7]
	ds_add_rtn_u32 v4, v85, v107
	global_store_dword v[8:9], v254, off
	v_fma_f32 v8, -v3, v10, 1.0
	v_fmac_f32_e32 v10, v8, v10
	v_div_scale_f32 v8, vcc, v2, v1, v2
	v_mul_f32_e32 v9, v8, v10
	v_fma_f32 v11, -v3, v9, v8
	v_fmac_f32_e32 v9, v11, v10
	v_fma_f32 v3, -v3, v9, v8
	v_div_fmas_f32 v3, v3, v10, v9
	v_div_fixup_f32 v1, v3, v1, v2
	v_mul_f32_e32 v1, 0x40200000, v1
	v_lshl_add_u64 v[2:3], s[58:59], 0, v[6:7]
	s_add_i32 s36, s40, s73
	global_store_dword v[2:3], v1, off
	s_waitcnt lgkmcnt(0)
	v_or_b32_e32 v1, v4, v86
	v_lshl_add_u32 v2, v5, 2, s36
	ds_write_b32 v2, v1
.LBB0_1893:
	s_or_b64 exec, exec, s[34:35]
	v_add_u32_e32 v1, s75, v84
	ds_read2st64_b32 v[2:3], v1 offset0:4 offset1:36
	s_mov_b32 s41, 0
	s_waitcnt lgkmcnt(0)
	v_add_f32_e32 v2, 0, v2
	v_add_f32_e32 v4, v2, v3
	ds_read2st64_b32 v[2:3], v1 offset0:68 offset1:100
	s_waitcnt lgkmcnt(0)
	v_add_f32_e32 v2, v4, v2
	v_add_f32_e32 v4, v2, v3
	ds_read2st64_b32 v[2:3], v1 offset0:132 offset1:164
	s_waitcnt lgkmcnt(0)
	v_add_f32_e32 v2, v4, v2
	v_add_f32_e32 v4, v2, v3
	ds_read2st64_b32 v[2:3], v1 offset0:196 offset1:228
	s_waitcnt lgkmcnt(0)
	v_add_f32_e32 v1, v4, v2
	v_add_f32_e32 v1, v1, v3
	v_mul_f32_e32 v2, 0xbfb8aa3b, v1
	v_fma_f32 v3, v1, s83, -v2
	v_rndne_f32_e32 v4, v2
	v_fmac_f32_e32 v3, 0xb2a5705f, v1
	v_sub_f32_e32 v2, v2, v4
	v_add_f32_e32 v2, v2, v3
	v_exp_f32_e32 v2, v2
	v_cvt_i32_f32_e32 v3, v4
	v_cmp_nlt_f32_e32 vcc, s84, v1
	v_ldexp_f32 v2, v2, v3
	s_nop 0
	v_cndmask_b32_e32 v2, 0, v2, vcc
	v_cmp_ngt_f32_e32 vcc, s85, v1
	s_nop 1
	v_cndmask_b32_e32 v1, v109, v2, vcc
	v_add_f32_e32 v1, 1.0, v1
	v_div_scale_f32 v2, s[34:35], v1, v1, 1.0
	v_rcp_f32_e32 v3, v2
	s_nop 0
	v_fma_f32 v4, -v2, v3, 1.0
	v_fmac_f32_e32 v3, v4, v3
	v_div_scale_f32 v4, vcc, 1.0, v1, 1.0
	v_mul_f32_e32 v5, v4, v3
	v_fma_f32 v6, -v2, v5, v4
	v_fmac_f32_e32 v5, v6, v3
	v_fma_f32 v2, -v2, v5, v4
	v_div_fmas_f32 v2, v2, v3, v5
	v_div_fixup_f32 v2, v2, v1, 1.0
	v_mov_b32_e32 v1, v128
	v_add_f32_e32 v3, v1, v2
	ds_bpermute_b32 v1, v88, v3
	ds_bpermute_b32 v4, v89, v3
	ds_bpermute_b32 v5, v90, v3
	ds_bpermute_b32 v6, v95, v3
	s_waitcnt lgkmcnt(3)
	v_cmp_eq_f32_e64 s[34:35], v3, v1
	v_cmp_lt_f32_e32 vcc, v3, v1
	s_and_b64 s[34:35], s[4:5], s[34:35]
	s_or_b64 s[34:35], vcc, s[34:35]
	v_cndmask_b32_e64 v1, 0, 1, s[34:35]
	s_waitcnt lgkmcnt(2)
	v_cmp_eq_f32_e64 s[34:35], v3, v4
	v_cmp_lt_f32_e32 vcc, v3, v4
	s_and_b64 s[34:35], s[6:7], s[34:35]
	s_or_b64 s[34:35], vcc, s[34:35]
	v_cndmask_b32_e64 v4, 0, 1, s[34:35]
	s_waitcnt lgkmcnt(1)
	v_cmp_eq_f32_e64 s[34:35], v3, v5
	v_cmp_lt_f32_e32 vcc, v3, v5
	s_and_b64 s[34:35], s[8:9], s[34:35]
	s_or_b64 s[34:35], vcc, s[34:35]
	v_cndmask_b32_e64 v5, 0, 1, s[34:35]
	v_add3_u32 v1, v1, v4, v5
	ds_bpermute_b32 v4, v91, v3
	ds_bpermute_b32 v5, v92, v3
	s_waitcnt lgkmcnt(1)
	v_cmp_eq_f32_e64 s[34:35], v3, v4
	v_cmp_lt_f32_e32 vcc, v3, v4
	s_and_b64 s[34:35], s[10:11], s[34:35]
	s_or_b64 s[34:35], vcc, s[34:35]
	v_cndmask_b32_e64 v4, 0, 1, s[34:35]
	s_waitcnt lgkmcnt(0)
	v_cmp_eq_f32_e64 s[34:35], v3, v5
	v_cmp_lt_f32_e32 vcc, v3, v5
	s_and_b64 s[34:35], s[12:13], s[34:35]
	s_or_b64 s[34:35], vcc, s[34:35]
	v_cndmask_b32_e64 v5, 0, 1, s[34:35]
	v_add3_u32 v1, v1, v4, v5
	ds_bpermute_b32 v4, v93, v3
	ds_bpermute_b32 v5, v94, v3
	s_waitcnt lgkmcnt(1)
	v_cmp_eq_f32_e64 s[34:35], v3, v4
	v_cmp_lt_f32_e32 vcc, v3, v4
	s_and_b64 s[34:35], s[14:15], s[34:35]
	s_or_b64 s[34:35], vcc, s[34:35]
	v_cndmask_b32_e64 v4, 0, 1, s[34:35]
	s_waitcnt lgkmcnt(0)
	v_cmp_eq_f32_e64 s[34:35], v3, v5
	v_cmp_lt_f32_e32 vcc, v3, v5
	s_and_b64 s[34:35], s[16:17], s[34:35]
	s_or_b64 s[34:35], vcc, s[34:35]
	v_cmp_lt_f32_e32 vcc, v3, v6
	v_cndmask_b32_e64 v5, 0, 1, s[34:35]
	s_nop 0
	v_addc_co_u32_e32 v1, vcc, v1, v4, vcc
	v_add_u32_e32 v1, v1, v5
	v_cmp_gt_u32_e32 vcc, 2, v1
	s_nop 1
	v_cndmask_b32_e32 v1, 0, v3, vcc
	s_waitcnt lgkmcnt(0)
	s_nop 1
	v_add_f32_dpp v1, v1, v1 quad_perm:[1,0,3,2] row_mask:0xf bank_mask:0xf
	s_waitcnt lgkmcnt(0)
	s_nop 1
	v_add_f32_dpp v1, v1, v1 quad_perm:[2,3,0,1] row_mask:0xf bank_mask:0xf
	s_waitcnt lgkmcnt(0)
	s_nop 1
	v_add_f32_dpp v1, v1, v1 row_half_mirror row_mask:0xf bank_mask:0xf
	ds_bpermute_b32 v4, v87, v1
	ds_bpermute_b32 v5, v96, v1
	ds_bpermute_b32 v6, v97, v1
	ds_bpermute_b32 v7, v98, v1
	ds_bpermute_b32 v8, v99, v1
	s_waitcnt lgkmcnt(4)
	v_cmp_eq_f32_e64 s[34:35], v1, v4
	v_cmp_lt_f32_e32 vcc, v1, v4
	s_and_b64 s[34:35], s[18:19], s[34:35]
	s_or_b64 s[34:35], vcc, s[34:35]
	v_cndmask_b32_e64 v4, 0, 1, s[34:35]
	s_waitcnt lgkmcnt(3)
	v_cmp_eq_f32_e64 s[34:35], v1, v5
	v_cmp_lt_f32_e32 vcc, v1, v5
	s_and_b64 s[34:35], s[20:21], s[34:35]
	s_or_b64 s[34:35], vcc, s[34:35]
	v_cndmask_b32_e64 v5, 0, 1, s[34:35]
	s_waitcnt lgkmcnt(2)
	v_cmp_eq_f32_e64 s[34:35], v1, v6
	v_cmp_lt_f32_e32 vcc, v1, v6
	s_and_b64 s[34:35], s[22:23], s[34:35]
	s_or_b64 s[34:35], vcc, s[34:35]
	v_cndmask_b32_e64 v6, 0, 1, s[34:35]
	s_waitcnt lgkmcnt(1)
	v_cmp_eq_f32_e64 s[34:35], v1, v7
	v_cmp_lt_f32_e32 vcc, v1, v7
	s_and_b64 s[34:35], s[24:25], s[34:35]
	ds_bpermute_b32 v9, v100, v1
	s_or_b64 s[34:35], vcc, s[34:35]
	v_cndmask_b32_e64 v7, 0, 1, s[34:35]
	s_waitcnt lgkmcnt(1)
	v_cmp_eq_f32_e64 s[34:35], v1, v8
	v_cmp_lt_f32_e32 vcc, v1, v8
	s_and_b64 s[34:35], s[26:27], s[34:35]
	ds_bpermute_b32 v10, v101, v1
	s_or_b64 s[34:35], vcc, s[34:35]
	v_cndmask_b32_e64 v8, 0, 1, s[34:35]
	s_waitcnt lgkmcnt(1)
	v_cmp_eq_f32_e64 s[34:35], v1, v9
	ds_bpermute_b32 v11, v102, v1
	v_cmp_lt_f32_e32 vcc, v1, v9
	s_and_b64 s[34:35], s[28:29], s[34:35]
	s_or_b64 s[34:35], vcc, s[34:35]
	v_cndmask_b32_e64 v9, 0, 1, s[34:35]
	s_waitcnt lgkmcnt(1)
	v_cmp_eq_f32_e64 s[34:35], v1, v10
	v_cmp_lt_f32_e32 vcc, v1, v10
	s_and_b64 s[34:35], s[30:31], s[34:35]
	s_or_b64 s[34:35], vcc, s[34:35]
	s_waitcnt lgkmcnt(0)
	v_cmp_lt_f32_e32 vcc, v1, v11
	v_cndmask_b32_e64 v10, 0, 1, s[34:35]
	s_nop 0
	v_cndmask_b32_e64 v1, 0, 1, vcc
	v_add_u32_e32 v1, v5, v1
	v_add3_u32 v1, v1, v4, v6
	v_add3_u32 v1, v1, v7, v8
	v_add3_u32 v1, v1, v9, v10
	v_cmp_gt_u32_e32 vcc, 4, v1
	v_mov_b32_e32 v5, 0
	v_mov_b32_e32 v4, v104
	v_cndmask_b32_e32 v3, v110, v3, vcc

.Lrk_exit_2:
	v_cmp_gt_u32_e64 s[34:35], 8, v5
	s_and_b64 vcc, vcc, s[34:35]
	v_cndmask_b32_e32 v1, 0, v2, vcc
	s_waitcnt lgkmcnt(0)
	s_nop 1
	v_add_f32_dpp v1, v1, v1 quad_perm:[1,0,3,2] row_mask:0xf bank_mask:0xf
	s_waitcnt lgkmcnt(0)
	s_nop 1
	v_add_f32_dpp v1, v1, v1 quad_perm:[2,3,0,1] row_mask:0xf bank_mask:0xf
	s_waitcnt lgkmcnt(0)
	s_nop 1
	v_add_f32_dpp v1, v1, v1 row_half_mirror row_mask:0xf bank_mask:0xf
	s_waitcnt lgkmcnt(0)
	s_nop 1
	v_add_f32_dpp v1, v1, v1 row_mirror row_mask:0xf bank_mask:0xf
	s_waitcnt lgkmcnt(0)
	v_mov_b32_e32 v3, v1
	s_nop 1
	v_permlane16_swap_b32_e32 v3, v1
	v_add_f32_e32 v3, v1, v3
	ds_bpermute_b32 v4, v81, v3
	s_and_saveexec_b64 s[34:35], vcc
	s_cbranch_execz .LBB0_1897
	s_add_i32 s36, s74, s87
	s_waitcnt lgkmcnt(0)
	v_add_f32_e32 v1, v3, v4
	v_lshl_or_b32 v6, s36, 3, v5
	v_div_scale_f32 v3, s[36:37], v1, v1, v2
	v_rcp_f32_e32 v10, v3
	v_ashrrev_i32_e32 v7, 31, v6
	v_lshlrev_b64 v[6:7], 2, v[6:7]
	v_lshl_add_u64 v[8:9], s[56:57], 0, v[6:7]
	ds_add_rtn_u32 v4, v85, v107
	global_store_dword v[8:9], v254, off
	v_fma_f32 v8, -v3, v10, 1.0
	v_fmac_f32_e32 v10, v8, v10
	v_div_scale_f32 v8, vcc, v2, v1, v2
	v_mul_f32_e32 v9, v8, v10
	v_fma_f32 v11, -v3, v9, v8
	v_fmac_f32_e32 v9, v11, v10
	v_fma_f32 v3, -v3, v9, v8
	v_div_fmas_f32 v3, v3, v10, v9
	v_div_fixup_f32 v1, v3, v1, v2
	v_mul_f32_e32 v1, 0x40200000, v1
	v_lshl_add_u64 v[2:3], s[58:59], 0, v[6:7]
	s_add_i32 s36, s40, s77
	global_store_dword v[2:3], v1, off
	s_waitcnt lgkmcnt(0)
	v_or_b32_e32 v1, v4, v86
	v_lshl_add_u32 v2, v5, 2, s36
	ds_write_b32 v2, v1
.LBB0_1897:
	s_or_b64 exec, exec, s[34:35]
	v_add_u32_e32 v1, s79, v84
	ds_read2st64_b32 v[2:3], v1 offset0:4 offset1:36
	s_mov_b32 s41, 0
	s_waitcnt lgkmcnt(0)
	v_add_f32_e32 v2, 0, v2
	v_add_f32_e32 v4, v2, v3
	ds_read2st64_b32 v[2:3], v1 offset0:68 offset1:100
	s_waitcnt lgkmcnt(0)
	v_add_f32_e32 v2, v4, v2
	v_add_f32_e32 v4, v2, v3
	ds_read2st64_b32 v[2:3], v1 offset0:132 offset1:164
	s_waitcnt lgkmcnt(0)
	v_add_f32_e32 v2, v4, v2
	v_add_f32_e32 v4, v2, v3
	ds_read2st64_b32 v[2:3], v1 offset0:196 offset1:228
	s_waitcnt lgkmcnt(0)
	v_add_f32_e32 v1, v4, v2
	v_add_f32_e32 v1, v1, v3
	v_mul_f32_e32 v2, 0xbfb8aa3b, v1
	v_fma_f32 v3, v1, s83, -v2
	v_rndne_f32_e32 v4, v2
	v_fmac_f32_e32 v3, 0xb2a5705f, v1
	v_sub_f32_e32 v2, v2, v4
	v_add_f32_e32 v2, v2, v3
	v_exp_f32_e32 v2, v2
	v_cvt_i32_f32_e32 v3, v4
	v_cmp_nlt_f32_e32 vcc, s84, v1
	v_ldexp_f32 v2, v2, v3
	s_nop 0
	v_cndmask_b32_e32 v2, 0, v2, vcc
	v_cmp_ngt_f32_e32 vcc, s85, v1
	s_nop 1
	v_cndmask_b32_e32 v1, v109, v2, vcc
	v_add_f32_e32 v1, 1.0, v1
	v_div_scale_f32 v2, s[34:35], v1, v1, 1.0
	v_rcp_f32_e32 v3, v2
	s_nop 0
	v_fma_f32 v4, -v2, v3, 1.0
	v_fmac_f32_e32 v3, v4, v3
	v_div_scale_f32 v4, vcc, 1.0, v1, 1.0
	v_mul_f32_e32 v5, v4, v3
	v_fma_f32 v6, -v2, v5, v4
	v_fmac_f32_e32 v5, v6, v3
	v_fma_f32 v2, -v2, v5, v4
	v_div_fmas_f32 v2, v2, v3, v5
	v_div_fixup_f32 v2, v2, v1, 1.0
	v_mov_b32_e32 v1, v128
	v_add_f32_e32 v3, v1, v2
	ds_bpermute_b32 v1, v88, v3
	ds_bpermute_b32 v4, v89, v3
	ds_bpermute_b32 v5, v90, v3
	ds_bpermute_b32 v6, v95, v3
	s_waitcnt lgkmcnt(3)
	v_cmp_eq_f32_e64 s[34:35], v3, v1
	v_cmp_lt_f32_e32 vcc, v3, v1
	s_and_b64 s[34:35], s[4:5], s[34:35]
	s_or_b64 s[34:35], vcc, s[34:35]
	v_cndmask_b32_e64 v1, 0, 1, s[34:35]
	s_waitcnt lgkmcnt(2)
	v_cmp_eq_f32_e64 s[34:35], v3, v4
	v_cmp_lt_f32_e32 vcc, v3, v4
	s_and_b64 s[34:35], s[6:7], s[34:35]
	s_or_b64 s[34:35], vcc, s[34:35]
	v_cndmask_b32_e64 v4, 0, 1, s[34:35]
	s_waitcnt lgkmcnt(1)
	v_cmp_eq_f32_e64 s[34:35], v3, v5
	v_cmp_lt_f32_e32 vcc, v3, v5
	s_and_b64 s[34:35], s[8:9], s[34:35]
	s_or_b64 s[34:35], vcc, s[34:35]
	v_cndmask_b32_e64 v5, 0, 1, s[34:35]
	v_add3_u32 v1, v1, v4, v5
	ds_bpermute_b32 v4, v91, v3
	ds_bpermute_b32 v5, v92, v3
	s_waitcnt lgkmcnt(1)
	v_cmp_eq_f32_e64 s[34:35], v3, v4
	v_cmp_lt_f32_e32 vcc, v3, v4
	s_and_b64 s[34:35], s[10:11], s[34:35]
	s_or_b64 s[34:35], vcc, s[34:35]
	v_cndmask_b32_e64 v4, 0, 1, s[34:35]
	s_waitcnt lgkmcnt(0)
	v_cmp_eq_f32_e64 s[34:35], v3, v5
	v_cmp_lt_f32_e32 vcc, v3, v5
	s_and_b64 s[34:35], s[12:13], s[34:35]
	s_or_b64 s[34:35], vcc, s[34:35]
	v_cndmask_b32_e64 v5, 0, 1, s[34:35]
	v_add3_u32 v1, v1, v4, v5
	ds_bpermute_b32 v4, v93, v3
	ds_bpermute_b32 v5, v94, v3
	s_waitcnt lgkmcnt(1)
	v_cmp_eq_f32_e64 s[34:35], v3, v4
	v_cmp_lt_f32_e32 vcc, v3, v4
	s_and_b64 s[34:35], s[14:15], s[34:35]
	s_or_b64 s[34:35], vcc, s[34:35]
	v_cndmask_b32_e64 v4, 0, 1, s[34:35]
	s_waitcnt lgkmcnt(0)
	v_cmp_eq_f32_e64 s[34:35], v3, v5
	v_cmp_lt_f32_e32 vcc, v3, v5
	s_and_b64 s[34:35], s[16:17], s[34:35]
	s_or_b64 s[34:35], vcc, s[34:35]
	v_cmp_lt_f32_e32 vcc, v3, v6
	v_cndmask_b32_e64 v5, 0, 1, s[34:35]
	s_nop 0
	v_addc_co_u32_e32 v1, vcc, v1, v4, vcc
	v_add_u32_e32 v1, v1, v5
	v_cmp_gt_u32_e32 vcc, 2, v1
	s_nop 1
	v_cndmask_b32_e32 v1, 0, v3, vcc
	s_waitcnt lgkmcnt(0)
	s_nop 1
	v_add_f32_dpp v1, v1, v1 quad_perm:[1,0,3,2] row_mask:0xf bank_mask:0xf
	s_waitcnt lgkmcnt(0)
	s_nop 1
	v_add_f32_dpp v1, v1, v1 quad_perm:[2,3,0,1] row_mask:0xf bank_mask:0xf
	s_waitcnt lgkmcnt(0)
	s_nop 1
	v_add_f32_dpp v1, v1, v1 row_half_mirror row_mask:0xf bank_mask:0xf
	ds_bpermute_b32 v4, v87, v1
	ds_bpermute_b32 v5, v96, v1
	ds_bpermute_b32 v6, v97, v1
	ds_bpermute_b32 v7, v98, v1
	ds_bpermute_b32 v8, v99, v1
	s_waitcnt lgkmcnt(4)
	v_cmp_eq_f32_e64 s[34:35], v1, v4
	v_cmp_lt_f32_e32 vcc, v1, v4
	s_and_b64 s[34:35], s[18:19], s[34:35]
	s_or_b64 s[34:35], vcc, s[34:35]
	v_cndmask_b32_e64 v4, 0, 1, s[34:35]
	s_waitcnt lgkmcnt(3)
	v_cmp_eq_f32_e64 s[34:35], v1, v5
	v_cmp_lt_f32_e32 vcc, v1, v5
	s_and_b64 s[34:35], s[20:21], s[34:35]
	s_or_b64 s[34:35], vcc, s[34:35]
	v_cndmask_b32_e64 v5, 0, 1, s[34:35]
	s_waitcnt lgkmcnt(2)
	v_cmp_eq_f32_e64 s[34:35], v1, v6
	v_cmp_lt_f32_e32 vcc, v1, v6
	s_and_b64 s[34:35], s[22:23], s[34:35]
	s_or_b64 s[34:35], vcc, s[34:35]
	v_cndmask_b32_e64 v6, 0, 1, s[34:35]
	s_waitcnt lgkmcnt(1)
	v_cmp_eq_f32_e64 s[34:35], v1, v7
	v_cmp_lt_f32_e32 vcc, v1, v7
	s_and_b64 s[34:35], s[24:25], s[34:35]
	ds_bpermute_b32 v9, v100, v1
	s_or_b64 s[34:35], vcc, s[34:35]
	v_cndmask_b32_e64 v7, 0, 1, s[34:35]
	s_waitcnt lgkmcnt(1)
	v_cmp_eq_f32_e64 s[34:35], v1, v8
	v_cmp_lt_f32_e32 vcc, v1, v8
	s_and_b64 s[34:35], s[26:27], s[34:35]
	ds_bpermute_b32 v10, v101, v1
	s_or_b64 s[34:35], vcc, s[34:35]
	v_cndmask_b32_e64 v8, 0, 1, s[34:35]
	s_waitcnt lgkmcnt(1)
	v_cmp_eq_f32_e64 s[34:35], v1, v9
	ds_bpermute_b32 v11, v102, v1
	v_cmp_lt_f32_e32 vcc, v1, v9
	s_and_b64 s[34:35], s[28:29], s[34:35]
	s_or_b64 s[34:35], vcc, s[34:35]
	v_cndmask_b32_e64 v9, 0, 1, s[34:35]
	s_waitcnt lgkmcnt(1)
	v_cmp_eq_f32_e64 s[34:35], v1, v10
	v_cmp_lt_f32_e32 vcc, v1, v10
	s_and_b64 s[34:35], s[30:31], s[34:35]
	s_or_b64 s[34:35], vcc, s[34:35]
	s_waitcnt lgkmcnt(0)
	v_cmp_lt_f32_e32 vcc, v1, v11
	v_cndmask_b32_e64 v10, 0, 1, s[34:35]
	s_nop 0
	v_cndmask_b32_e64 v1, 0, 1, vcc
	v_add_u32_e32 v1, v5, v1
	v_add3_u32 v1, v1, v4, v6
	v_add3_u32 v1, v1, v7, v8
	v_add3_u32 v1, v1, v9, v10
	v_cmp_gt_u32_e32 vcc, 4, v1
	v_mov_b32_e32 v5, 0
	v_mov_b32_e32 v4, v104
	v_cndmask_b32_e32 v3, v110, v3, vcc

.Lrk_exit_3:
	v_cmp_gt_u32_e64 s[34:35], 8, v5
	s_and_b64 vcc, vcc, s[34:35]
	v_cndmask_b32_e32 v1, 0, v2, vcc
	s_waitcnt lgkmcnt(0)
	s_nop 1
	v_add_f32_dpp v1, v1, v1 quad_perm:[1,0,3,2] row_mask:0xf bank_mask:0xf
	s_waitcnt lgkmcnt(0)
	s_nop 1
	v_add_f32_dpp v1, v1, v1 quad_perm:[2,3,0,1] row_mask:0xf bank_mask:0xf
	s_waitcnt lgkmcnt(0)
	s_nop 1
	v_add_f32_dpp v1, v1, v1 row_half_mirror row_mask:0xf bank_mask:0xf
	s_waitcnt lgkmcnt(0)
	s_nop 1
	v_add_f32_dpp v1, v1, v1 row_mirror row_mask:0xf bank_mask:0xf
	s_waitcnt lgkmcnt(0)
	v_mov_b32_e32 v3, v1
	s_nop 1
	v_permlane16_swap_b32_e32 v3, v1
	v_add_f32_e32 v3, v1, v3
	ds_bpermute_b32 v4, v81, v3
	s_and_saveexec_b64 s[34:35], vcc
	s_cbranch_execz .LBB0_1874
	s_add_i32 s36, s78, s87
	s_waitcnt lgkmcnt(0)
	v_add_f32_e32 v1, v3, v4
	v_lshl_or_b32 v6, s36, 3, v5
	v_div_scale_f32 v3, s[36:37], v1, v1, v2
	v_rcp_f32_e32 v10, v3
	v_ashrrev_i32_e32 v7, 31, v6
	v_lshlrev_b64 v[6:7], 2, v[6:7]
	v_lshl_add_u64 v[8:9], s[56:57], 0, v[6:7]
	ds_add_rtn_u32 v4, v85, v107
	global_store_dword v[8:9], v254, off
	v_fma_f32 v8, -v3, v10, 1.0
	v_fmac_f32_e32 v10, v8, v10
	v_div_scale_f32 v8, vcc, v2, v1, v2
	v_mul_f32_e32 v9, v8, v10
	v_fma_f32 v11, -v3, v9, v8
	v_fmac_f32_e32 v9, v11, v10
	v_fma_f32 v3, -v3, v9, v8
	v_div_fmas_f32 v3, v3, v10, v9
	v_div_fixup_f32 v1, v3, v1, v2
	v_mul_f32_e32 v1, 0x40200000, v1
	v_lshl_add_u64 v[2:3], s[58:59], 0, v[6:7]
	s_add_i32 s40, s40, s80
	global_store_dword v[2:3], v1, off
	s_waitcnt lgkmcnt(0)
	v_or_b32_e32 v1, v4, v86
	v_lshl_add_u32 v2, v5, 2, s40
	ds_write_b32 v2, v1
	s_branch .LBB0_1874
